# v56 + lever 7 in the attention tile loops: 31-add row-sum chains replaced by 15 v_pk_add_f32 + 1 add (18 sites, 270 VALU fewer), f32 throughout
# baseline (speedup 1.0000x reference)
.LBB0_953:
	v_add_u32_e32 v168, s34, v240
	ds_read_b64_tr_b16 v[164:165], v168 offset:24576
	ds_read_b64_tr_b16 v[166:167], v168 offset:25088
	v_pk_add_f32 v[254:255], v[52:53], v[54:55]
	v_pk_add_f32 v[254:255], v[254:255], v[56:57]
	s_waitcnt lgkmcnt(9)
	v_mfma_f32_32x32x16_bf16 v[68:83], v[160:163], v[116:119], 0
	v_cvt_pk_bf16_f32 v128, v52, v53
	v_cvt_pk_bf16_f32 v129, v54, v55
	ds_read_b64_tr_b16 v[160:161], v168 offset:28672
	ds_read_b64_tr_b16 v[162:163], v168 offset:29184
	v_pk_add_f32 v[254:255], v[254:255], v[58:59]
	v_pk_add_f32 v[254:255], v[254:255], v[60:61]
	v_cvt_pk_bf16_f32 v130, v56, v57
	v_cvt_pk_bf16_f32 v131, v58, v59
	s_waitcnt lgkmcnt(10)
	v_mfma_f32_32x32x16_bf16 v[84:99], v[152:155], v[116:119], 0
	ds_read_b64_tr_b16 v[152:153], v168 offset:25600
	ds_read_b64_tr_b16 v[154:155], v168 offset:26112
	s_waitcnt lgkmcnt(11)
	v_mfma_f32_32x32x16_bf16 v[68:83], v[156:159], v[108:111], v[68:83]
	v_pk_add_f32 v[254:255], v[254:255], v[62:63]
	v_pk_add_f32 v[254:255], v[254:255], v[64:65]
	v_cvt_pk_bf16_f32 v124, v60, v61
	v_cvt_pk_bf16_f32 v125, v62, v63
	ds_read_b64_tr_b16 v[156:157], v168 offset:29696
	ds_read_b64_tr_b16 v[158:159], v168 offset:30208
	v_pk_add_f32 v[254:255], v[254:255], v[66:67]
	v_pk_add_f32 v[254:255], v[254:255], v[36:37]
	v_cvt_pk_bf16_f32 v126, v64, v65
	v_cvt_pk_bf16_f32 v127, v66, v67
	s_waitcnt lgkmcnt(12)
	v_mfma_f32_32x32x16_bf16 v[84:99], v[148:151], v[108:111], v[84:99]
	ds_read_b64_tr_b16 v[148:149], v168 offset:26624
	ds_read_b64_tr_b16 v[150:151], v168 offset:27136
	s_waitcnt lgkmcnt(13)
	v_mfma_f32_32x32x16_bf16 v[68:83], v[144:147], v[104:107], v[68:83]
	v_pk_add_f32 v[254:255], v[254:255], v[38:39]
	v_pk_add_f32 v[254:255], v[254:255], v[40:41]
	v_cvt_pk_bf16_f32 v120, v36, v37
	v_cvt_pk_bf16_f32 v121, v38, v39
	ds_read_b64_tr_b16 v[144:145], v168 offset:30720
	ds_read_b64_tr_b16 v[146:147], v168 offset:31232
	v_pk_add_f32 v[254:255], v[254:255], v[42:43]
	v_pk_add_f32 v[254:255], v[254:255], v[44:45]
	v_cvt_pk_bf16_f32 v122, v40, v41
	v_cvt_pk_bf16_f32 v123, v42, v43
	s_waitcnt lgkmcnt(14)
	v_mfma_f32_32x32x16_bf16 v[84:99], v[140:143], v[104:107], v[84:99]
	ds_read_b64_tr_b16 v[140:141], v168 offset:27648
	ds_read_b64_tr_b16 v[142:143], v168 offset:28160
	s_waitcnt lgkmcnt(14)
	v_mfma_f32_32x32x16_bf16 v[68:83], v[136:139], v[100:103], v[68:83]
	v_pk_add_f32 v[254:255], v[254:255], v[46:47]
	v_pk_add_f32 v[254:255], v[254:255], v[48:49]
	v_cvt_pk_bf16_f32 v112, v44, v45
	v_cvt_pk_bf16_f32 v113, v46, v47
	ds_read_b64_tr_b16 v[136:137], v168 offset:31744
	ds_read_b64_tr_b16 v[138:139], v168 offset:32256
	v_pk_add_f32 v[254:255], v[254:255], v[50:51]
	v_add_f32_e32 v36, v254, v255
	v_mfma_f32_32x32x16_bf16 v[84:99], v[132:135], v[100:103], v[84:99]
	v_add_f32_e32 v133, 0, v36
	v_cvt_pk_bf16_f32 v114, v48, v49
	v_cvt_pk_bf16_f32 v115, v50, v51
	v_lshl_add_u64 v[184:185], v[182:183], 0, s[18:19]
	s_mov_b64 s[34:35], 0x13080000
	v_lshl_add_u64 v[36:37], v[184:185], 0, s[34:35]
	s_add_i32 s34, s67, s58
	s_mov_b32 s35, m0
	s_mov_b32 m0, s34
	s_nop 0
	global_load_lds_dwordx4 v[36:37], off
	s_mov_b32 m0, s35
	v_lshl_add_u64 v[186:187], v[180:181], 0, s[18:19]
	s_mov_b64 s[34:35], 0x15040000
	v_lshl_add_u64 v[36:37], v[186:187], 0, s[34:35]
	s_add_i32 s34, s7, s59
	s_mov_b32 s35, m0
	s_mov_b32 m0, s34
	s_nop 0
	global_load_lds_dwordx4 v[36:37], off
	s_mov_b32 m0, s35
	ds_read_b128 v[36:39], v191
	ds_read_b128 v[40:43], v191 offset:32
	ds_read_b128 v[44:47], v191 offset:128
	v_sub_f32_e32 v132, v237, v239
	v_add_f32_e32 v192, v241, v133
	s_waitcnt lgkmcnt(2)
	v_pk_add_f32 v[36:37], v[132:133], v[36:37] op_sel_hi:[0,1] neg_lo:[0,1] neg_hi:[0,1]
	v_pk_add_f32 v[38:39], v[132:133], v[38:39] op_sel_hi:[0,1] neg_lo:[0,1] neg_hi:[0,1]
	v_pk_add_f32 v[52:53], v[68:69], v[36:37]
	s_waitcnt lgkmcnt(0)
	v_pk_add_f32 v[36:37], v[132:133], v[44:45] op_sel_hi:[0,1] neg_lo:[0,1] neg_hi:[0,1]
	v_pk_add_f32 v[54:55], v[70:71], v[38:39]
	v_pk_add_f32 v[38:39], v[132:133], v[46:47] op_sel_hi:[0,1] neg_lo:[0,1] neg_hi:[0,1]
	ds_read_b128 v[44:47], v191 offset:160
	v_pk_add_f32 v[40:41], v[132:133], v[40:41] op_sel_hi:[0,1] neg_lo:[0,1] neg_hi:[0,1]
	v_pk_add_f32 v[42:43], v[132:133], v[42:43] op_sel_hi:[0,1] neg_lo:[0,1] neg_hi:[0,1]
	v_pk_add_f32 v[56:57], v[72:73], v[40:41]
	v_pk_add_f32 v[58:59], v[74:75], v[42:43]
	s_waitcnt lgkmcnt(0)
	v_pk_add_f32 v[40:41], v[132:133], v[44:45] op_sel_hi:[0,1] neg_lo:[0,1] neg_hi:[0,1]
	v_pk_add_f32 v[42:43], v[132:133], v[46:47] op_sel_hi:[0,1] neg_lo:[0,1] neg_hi:[0,1]
	ds_read_b128 v[44:47], v191 offset:64
	ds_read_b128 v[48:51], v191 offset:192
	v_pk_add_f32 v[36:37], v[84:85], v[36:37]
	v_pk_add_f32 v[38:39], v[86:87], v[38:39]
	v_pk_add_f32 v[40:41], v[88:89], v[40:41]
	s_waitcnt lgkmcnt(1)
	v_pk_add_f32 v[44:45], v[132:133], v[44:45] op_sel_hi:[0,1] neg_lo:[0,1] neg_hi:[0,1]
	v_pk_add_f32 v[46:47], v[132:133], v[46:47] op_sel_hi:[0,1] neg_lo:[0,1] neg_hi:[0,1]
	v_pk_add_f32 v[60:61], v[76:77], v[44:45]
	s_waitcnt lgkmcnt(0)
	v_pk_add_f32 v[44:45], v[132:133], v[48:49] op_sel_hi:[0,1] neg_lo:[0,1] neg_hi:[0,1]
	v_pk_add_f32 v[62:63], v[78:79], v[46:47]
	v_pk_add_f32 v[46:47], v[132:133], v[50:51] op_sel_hi:[0,1] neg_lo:[0,1] neg_hi:[0,1]
	ds_read_b128 v[48:51], v191 offset:96
	ds_read_b128 v[66:69], v191 offset:224
	v_pk_add_f32 v[42:43], v[90:91], v[42:43]
	v_pk_add_f32 v[44:45], v[92:93], v[44:45]
	v_pk_add_f32 v[46:47], v[94:95], v[46:47]
	s_waitcnt lgkmcnt(1)
	v_pk_add_f32 v[48:49], v[132:133], v[48:49] op_sel_hi:[0,1] neg_lo:[0,1] neg_hi:[0,1]
	v_pk_add_f32 v[50:51], v[132:133], v[50:51] op_sel_hi:[0,1] neg_lo:[0,1] neg_hi:[0,1]
	v_pk_add_f32 v[64:65], v[80:81], v[48:49]
	s_waitcnt lgkmcnt(0)
	v_pk_add_f32 v[48:49], v[132:133], v[66:67] op_sel_hi:[0,1] neg_lo:[0,1] neg_hi:[0,1]
	v_pk_add_f32 v[66:67], v[82:83], v[50:51]
	v_pk_add_f32 v[50:51], v[132:133], v[68:69] op_sel_hi:[0,1] neg_lo:[0,1] neg_hi:[0,1]
	v_max_f32_e32 v68, v52, v53
	v_max3_f32 v69, v54, v55, v37
	v_max3_f32 v68, v68, v36, v38
	v_max3_f32 v68, v68, v39, v56
	v_max3_f32 v69, v69, v58, v59
	v_max3_f32 v68, v68, v57, v40
	v_max3_f32 v69, v69, v42, v43
	v_max3_f32 v68, v68, v41, v60
	v_max3_f32 v69, v69, v62, v63
	v_max3_f32 v68, v68, v61, v44
	v_max3_f32 v69, v69, v46, v47
	v_pk_add_f32 v[48:49], v[96:97], v[48:49]
	v_pk_add_f32 v[50:51], v[98:99], v[50:51]
	v_max3_f32 v68, v68, v45, v64
	v_max3_f32 v69, v69, v66, v67
	v_max3_f32 v68, v68, v65, v48
	v_max3_f32 v69, v69, v50, v51
	v_max3_f32 v68, v68, v49, v69
	v_mov_b32_e32 v69, v68
	s_nop 1
	v_permlane32_swap_b32_e32 v68, v69
	v_max_f32_e32 v69, v69, v69
	v_max_f32_e32 v68, v68, v68
	v_max_f32_e32 v68, v68, v69
	v_cmp_lt_f32_e32 vcc, s94, v68
	s_cmp_lg_u64 vcc, 0
	s_cselect_b64 s[34:35], -1, 0
	s_cbranch_vccnz .LBB0_961

.LBB0_956:
	s_add_i32 s34, s7, 0x2000
	s_cmpk_lg_i32 s7, 0x4000
	s_cselect_b32 s61, s34, 0
	v_add_u32_e32 v174, s67, v240
	ds_read_b64_tr_b16 v[144:145], v174 offset:24576
	ds_read_b64_tr_b16 v[146:147], v174 offset:25088
	v_pk_add_f32 v[254:255], v[52:53], v[54:55]
	v_pk_add_f32 v[254:255], v[254:255], v[56:57]
	s_waitcnt lgkmcnt(9)
	v_mfma_f32_32x32x16_bf16 v[68:83], v[68:71], v[116:119], 0
	v_cvt_pk_bf16_f32 v128, v52, v53
	v_cvt_pk_bf16_f32 v129, v54, v55
	ds_read_b64_tr_b16 v[140:141], v174 offset:28672
	ds_read_b64_tr_b16 v[142:143], v174 offset:29184
	v_pk_add_f32 v[254:255], v[254:255], v[58:59]
	v_pk_add_f32 v[254:255], v[254:255], v[60:61]
	v_cvt_pk_bf16_f32 v130, v56, v57
	v_cvt_pk_bf16_f32 v131, v58, v59
	s_waitcnt lgkmcnt(10)
	v_mfma_f32_32x32x16_bf16 v[84:99], v[84:87], v[116:119], 0
	ds_read_b64_tr_b16 v[132:133], v174 offset:25600
	ds_read_b64_tr_b16 v[134:135], v174 offset:26112
	s_waitcnt lgkmcnt(11)
	v_mfma_f32_32x32x16_bf16 v[68:83], v[168:171], v[108:111], v[68:83]
	v_pk_add_f32 v[254:255], v[254:255], v[62:63]
	v_pk_add_f32 v[254:255], v[254:255], v[64:65]
	v_cvt_pk_bf16_f32 v124, v60, v61
	v_cvt_pk_bf16_f32 v125, v62, v63
	ds_read_b64_tr_b16 v[136:137], v174 offset:29696
	ds_read_b64_tr_b16 v[138:139], v174 offset:30208
	v_pk_add_f32 v[254:255], v[254:255], v[66:67]
	v_pk_add_f32 v[254:255], v[254:255], v[36:37]
	v_cvt_pk_bf16_f32 v126, v64, v65
	v_cvt_pk_bf16_f32 v127, v66, v67
	s_waitcnt lgkmcnt(12)
	v_mfma_f32_32x32x16_bf16 v[84:99], v[164:167], v[108:111], v[84:99]
	ds_read_b64_tr_b16 v[176:177], v174 offset:26624
	ds_read_b64_tr_b16 v[178:179], v174 offset:27136
	s_waitcnt lgkmcnt(13)
	v_mfma_f32_32x32x16_bf16 v[68:83], v[160:163], v[104:107], v[68:83]
	v_pk_add_f32 v[254:255], v[254:255], v[38:39]
	v_pk_add_f32 v[254:255], v[254:255], v[40:41]
	v_cvt_pk_bf16_f32 v120, v36, v37
	v_cvt_pk_bf16_f32 v121, v38, v39
	ds_read_b64_tr_b16 v[164:165], v174 offset:30720
	ds_read_b64_tr_b16 v[166:167], v174 offset:31232
	v_pk_add_f32 v[254:255], v[254:255], v[42:43]
	v_pk_add_f32 v[254:255], v[254:255], v[44:45]
	v_cvt_pk_bf16_f32 v122, v40, v41
	v_cvt_pk_bf16_f32 v123, v42, v43
	s_waitcnt lgkmcnt(14)
	v_mfma_f32_32x32x16_bf16 v[84:99], v[152:155], v[104:107], v[84:99]
	ds_read_b64_tr_b16 v[168:169], v174 offset:27648
	ds_read_b64_tr_b16 v[170:171], v174 offset:28160
	s_waitcnt lgkmcnt(14)
	v_mfma_f32_32x32x16_bf16 v[68:83], v[156:159], v[100:103], v[68:83]
	v_pk_add_f32 v[254:255], v[254:255], v[46:47]
	v_pk_add_f32 v[254:255], v[254:255], v[48:49]
	v_cvt_pk_bf16_f32 v112, v44, v45
	v_cvt_pk_bf16_f32 v113, v46, v47
	ds_read_b64_tr_b16 v[172:173], v174 offset:31744
	ds_read_b64_tr_b16 v[174:175], v174 offset:32256
	v_pk_add_f32 v[254:255], v[254:255], v[50:51]
	v_add_f32_e32 v36, v254, v255
	v_mfma_f32_32x32x16_bf16 v[84:99], v[148:151], v[100:103], v[84:99]
	v_add_f32_e32 v149, 0, v36
	v_cvt_pk_bf16_f32 v114, v48, v49
	v_cvt_pk_bf16_f32 v115, v50, v51
	s_mov_b64 s[34:35], 0x130a0000
	v_lshl_add_u64 v[36:37], v[184:185], 0, s[34:35]
	s_add_i32 s34, s7, s58
	s_mov_b32 s35, m0
	s_mov_b32 m0, s34
	s_nop 0
	global_load_lds_dwordx4 v[36:37], off
	s_mov_b32 m0, s35
	s_mov_b64 s[34:35], 0x15060000
	v_lshl_add_u64 v[36:37], v[186:187], 0, s[34:35]
	s_add_i32 s34, s61, s59
	s_mov_b32 s35, m0
	s_mov_b32 m0, s34
	s_nop 0
	global_load_lds_dwordx4 v[36:37], off
	s_mov_b32 m0, s35
	ds_read_b128 v[36:39], v191 offset:256
	ds_read_b128 v[40:43], v191 offset:288
	ds_read_b128 v[44:47], v191 offset:384
	v_sub_f32_e32 v148, v237, v239
	v_add_f32_e32 v241, v192, v149
	s_waitcnt lgkmcnt(2)
	v_pk_add_f32 v[36:37], v[148:149], v[36:37] op_sel_hi:[0,1] neg_lo:[0,1] neg_hi:[0,1]
	v_pk_add_f32 v[38:39], v[148:149], v[38:39] op_sel_hi:[0,1] neg_lo:[0,1] neg_hi:[0,1]
	v_pk_add_f32 v[52:53], v[68:69], v[36:37]
	s_waitcnt lgkmcnt(0)
	v_pk_add_f32 v[36:37], v[148:149], v[44:45] op_sel_hi:[0,1] neg_lo:[0,1] neg_hi:[0,1]
	v_pk_add_f32 v[54:55], v[70:71], v[38:39]
	v_pk_add_f32 v[38:39], v[148:149], v[46:47] op_sel_hi:[0,1] neg_lo:[0,1] neg_hi:[0,1]
	ds_read_b128 v[44:47], v191 offset:416
	v_pk_add_f32 v[40:41], v[148:149], v[40:41] op_sel_hi:[0,1] neg_lo:[0,1] neg_hi:[0,1]
	v_pk_add_f32 v[42:43], v[148:149], v[42:43] op_sel_hi:[0,1] neg_lo:[0,1] neg_hi:[0,1]
	v_pk_add_f32 v[56:57], v[72:73], v[40:41]
	v_pk_add_f32 v[58:59], v[74:75], v[42:43]
	s_waitcnt lgkmcnt(0)
	v_pk_add_f32 v[40:41], v[148:149], v[44:45] op_sel_hi:[0,1] neg_lo:[0,1] neg_hi:[0,1]
	v_pk_add_f32 v[42:43], v[148:149], v[46:47] op_sel_hi:[0,1] neg_lo:[0,1] neg_hi:[0,1]
	ds_read_b128 v[44:47], v191 offset:320
	ds_read_b128 v[48:51], v191 offset:448
	v_pk_add_f32 v[36:37], v[84:85], v[36:37]
	v_pk_add_f32 v[38:39], v[86:87], v[38:39]
	v_pk_add_f32 v[40:41], v[88:89], v[40:41]
	s_waitcnt lgkmcnt(1)
	v_pk_add_f32 v[44:45], v[148:149], v[44:45] op_sel_hi:[0,1] neg_lo:[0,1] neg_hi:[0,1]
	v_pk_add_f32 v[46:47], v[148:149], v[46:47] op_sel_hi:[0,1] neg_lo:[0,1] neg_hi:[0,1]
	v_pk_add_f32 v[60:61], v[76:77], v[44:45]
	s_waitcnt lgkmcnt(0)
	v_pk_add_f32 v[44:45], v[148:149], v[48:49] op_sel_hi:[0,1] neg_lo:[0,1] neg_hi:[0,1]
	v_pk_add_f32 v[62:63], v[78:79], v[46:47]
	v_pk_add_f32 v[46:47], v[148:149], v[50:51] op_sel_hi:[0,1] neg_lo:[0,1] neg_hi:[0,1]
	ds_read_b128 v[48:51], v191 offset:352
	ds_read_b128 v[66:69], v191 offset:480
	v_pk_add_f32 v[42:43], v[90:91], v[42:43]
	v_pk_add_f32 v[44:45], v[92:93], v[44:45]
	v_pk_add_f32 v[46:47], v[94:95], v[46:47]
	s_waitcnt lgkmcnt(1)
	v_pk_add_f32 v[48:49], v[148:149], v[48:49] op_sel_hi:[0,1] neg_lo:[0,1] neg_hi:[0,1]
	v_pk_add_f32 v[50:51], v[148:149], v[50:51] op_sel_hi:[0,1] neg_lo:[0,1] neg_hi:[0,1]
	v_pk_add_f32 v[64:65], v[80:81], v[48:49]
	s_waitcnt lgkmcnt(0)
	v_pk_add_f32 v[48:49], v[148:149], v[66:67] op_sel_hi:[0,1] neg_lo:[0,1] neg_hi:[0,1]
	v_pk_add_f32 v[66:67], v[82:83], v[50:51]
	v_pk_add_f32 v[50:51], v[148:149], v[68:69] op_sel_hi:[0,1] neg_lo:[0,1] neg_hi:[0,1]
	v_max_f32_e32 v68, v52, v53
	v_max3_f32 v69, v54, v55, v37
	v_max3_f32 v68, v68, v36, v38
	v_max3_f32 v68, v68, v39, v56
	v_max3_f32 v69, v69, v58, v59
	v_max3_f32 v68, v68, v57, v40
	v_max3_f32 v69, v69, v42, v43
	v_max3_f32 v68, v68, v41, v60
	v_max3_f32 v69, v69, v62, v63
	v_max3_f32 v68, v68, v61, v44
	v_max3_f32 v69, v69, v46, v47
	v_pk_add_f32 v[48:49], v[96:97], v[48:49]
	v_pk_add_f32 v[50:51], v[98:99], v[50:51]
	v_max3_f32 v68, v68, v45, v64
	v_max3_f32 v69, v69, v66, v67
	v_max3_f32 v68, v68, v65, v48
	v_max3_f32 v69, v69, v50, v51
	v_max3_f32 v68, v68, v49, v69
	v_mov_b32_e32 v69, v68
	s_nop 1
	v_permlane32_swap_b32_e32 v68, v69
	v_max_f32_e32 v69, v69, v69
	v_max_f32_e32 v68, v68, v68
	v_max_f32_e32 v68, v68, v69
	v_cmp_lt_f32_e32 vcc, s94, v68
	s_cmp_lg_u64 vcc, 0
	s_cselect_b64 s[34:35], -1, 0
	s_cbranch_vccnz .LBB0_964

.LBB0_969:
	s_mov_b64 s[64:65], 0x80
	v_add_u32_e32 v2, s38, v240
	ds_read_b64_tr_b16 v[164:165], v2 offset:24576
	ds_read_b64_tr_b16 v[166:167], v2 offset:25088
	v_pk_add_f32 v[254:255], v[52:53], v[54:55]
	v_pk_add_f32 v[254:255], v[254:255], v[56:57]
	v_cvt_pk_bf16_f32 v128, v52, v53
	v_cvt_pk_bf16_f32 v129, v54, v55
	s_waitcnt lgkmcnt(3)
	v_mfma_f32_32x32x16_bf16 v[84:99], v[160:163], v[116:119], 0
	ds_read_b64_tr_b16 v[160:161], v2 offset:28672
	ds_read_b64_tr_b16 v[162:163], v2 offset:29184
	v_pk_add_f32 v[254:255], v[254:255], v[58:59]
	s_waitcnt lgkmcnt(4)
	v_mfma_f32_32x32x16_bf16 v[68:83], v[152:155], v[116:119], 0
	v_pk_add_f32 v[254:255], v[254:255], v[60:61]
	v_cvt_pk_bf16_f32 v130, v56, v57
	v_cvt_pk_bf16_f32 v131, v58, v59
	ds_read_b64_tr_b16 v[116:117], v2 offset:25600
	ds_read_b64_tr_b16 v[118:119], v2 offset:26112
	v_pk_add_f32 v[254:255], v[254:255], v[62:63]
	v_pk_add_f32 v[254:255], v[254:255], v[64:65]
	v_cvt_pk_bf16_f32 v124, v60, v61
	v_cvt_pk_bf16_f32 v125, v62, v63
	v_mfma_f32_32x32x16_bf16 v[84:99], v[156:159], v[108:111], v[84:99]
	ds_read_b64_tr_b16 v[152:153], v2 offset:29696
	ds_read_b64_tr_b16 v[154:155], v2 offset:30208
	v_mfma_f32_32x32x16_bf16 v[68:83], v[148:151], v[108:111], v[68:83]
	v_pk_add_f32 v[254:255], v[254:255], v[66:67]
	v_pk_add_f32 v[254:255], v[254:255], v[36:37]
	v_cvt_pk_bf16_f32 v126, v64, v65
	v_cvt_pk_bf16_f32 v127, v66, v67
	ds_read_b64_tr_b16 v[108:109], v2 offset:26624
	ds_read_b64_tr_b16 v[110:111], v2 offset:27136
	v_pk_add_f32 v[254:255], v[254:255], v[38:39]
	v_pk_add_f32 v[254:255], v[254:255], v[40:41]
	v_cvt_pk_bf16_f32 v120, v36, v37
	v_cvt_pk_bf16_f32 v121, v38, v39
	v_mfma_f32_32x32x16_bf16 v[84:99], v[144:147], v[104:107], v[84:99]
	ds_read_b64_tr_b16 v[144:145], v2 offset:30720
	ds_read_b64_tr_b16 v[146:147], v2 offset:31232
	v_mfma_f32_32x32x16_bf16 v[68:83], v[140:143], v[104:107], v[68:83]
	v_pk_add_f32 v[254:255], v[254:255], v[42:43]
	v_pk_add_f32 v[254:255], v[254:255], v[44:45]
	v_cvt_pk_bf16_f32 v122, v40, v41
	v_cvt_pk_bf16_f32 v123, v42, v43
	ds_read_b64_tr_b16 v[104:105], v2 offset:27648
	ds_read_b64_tr_b16 v[106:107], v2 offset:28160
	v_pk_add_f32 v[254:255], v[254:255], v[46:47]
	v_pk_add_f32 v[254:255], v[254:255], v[48:49]
	v_cvt_pk_bf16_f32 v112, v44, v45
	v_cvt_pk_bf16_f32 v113, v46, v47
	v_mfma_f32_32x32x16_bf16 v[84:99], v[136:139], v[100:103], v[84:99]
	ds_read_b64_tr_b16 v[136:137], v2 offset:31744
	ds_read_b64_tr_b16 v[138:139], v2 offset:32256
	v_mfma_f32_32x32x16_bf16 v[68:83], v[132:135], v[100:103], v[68:83]
	v_pk_add_f32 v[254:255], v[254:255], v[50:51]
	v_add_f32_e32 v2, v254, v255
	v_add_f32_e32 v2, 0, v2
	v_cvt_pk_bf16_f32 v114, v48, v49
	v_cvt_pk_bf16_f32 v115, v50, v51
	v_lshl_add_u32 v64, v235, 2, s57
	ds_read_b128 v[36:39], v64 offset:768
	ds_read_b128 v[40:43], v64 offset:800
	ds_read_b128 v[44:47], v64 offset:896
	ds_read_b128 v[48:51], v64 offset:928
	ds_read_b128 v[52:55], v64 offset:832
	ds_read_b128 v[56:59], v64 offset:864
	ds_read_b128 v[60:63], v64 offset:960
	ds_read_b128 v[64:67], v64 offset:992
	v_sub_f32_e32 v100, v237, v239
	s_waitcnt lgkmcnt(7)
	v_sub_f32_e32 v37, v100, v37
	v_sub_f32_e32 v36, v100, v36
	s_waitcnt lgkmcnt(3)
	v_sub_f32_e32 v53, v100, v53
	v_sub_f32_e32 v52, v100, v52
	v_sub_f32_e32 v39, v100, v39
	v_sub_f32_e32 v38, v100, v38
	v_pk_add_f32 v[38:39], v[86:87], v[38:39]
	v_pk_add_f32 v[86:87], v[92:93], v[52:53]
	v_pk_add_f32 v[52:53], v[84:85], v[36:37]
	v_sub_f32_e32 v37, v100, v45
	v_sub_f32_e32 v36, v100, v44
	s_waitcnt lgkmcnt(0)
; __device__ __forceinline__ void cmask(f32x16&p0,f32x16&p1,int jb,int qrel,int hi){
;   const float NEG=-INFINITY; int kb=64*jb+4*hi;
;   #pragma unroll
;   for(int r=0;r<16;++r){int kv=kb+(r&3)+8*(r>>2); if(kv>qrel)p0[r]=NEG; if(kv+32>qrel)p1[r]=NEG;}
; }
	v_sub_f32_e32 v45, v100, v67
	v_sub_f32_e32 v44, v100, v66
	v_sub_f32_e32 v47, v100, v47
	v_sub_f32_e32 v46, v100, v46
	v_pk_add_f32 v[46:47], v[70:71], v[46:47]
	v_pk_add_f32 v[70:71], v[82:83], v[44:45]
	v_or_b32_e32 v45, 0xe0, v235
	v_pk_add_f32 v[36:37], v[68:69], v[36:37]
	v_or_b32_e32 v44, 0xc0, v235
	v_cmp_le_i32_e32 vcc, v45, v236
	v_sub_f32_e32 v55, v100, v55
	v_sub_f32_e32 v54, v100, v54
	v_cndmask_b32_e32 v36, v222, v36, vcc
	v_cmp_lt_i32_e32 vcc, v44, v236
	v_sub_f32_e32 v41, v100, v41
	v_sub_f32_e32 v40, v100, v40
	v_cndmask_b32_e32 v53, v222, v53, vcc
	v_cmp_le_i32_e32 vcc, v44, v236
	v_or_b32_e32 v44, 0xe1, v235
	v_pk_add_f32 v[40:41], v[88:89], v[40:41]
	v_cndmask_b32_e32 v52, v222, v52, vcc
	v_cmp_le_i32_e32 vcc, v44, v236
	v_or_b32_e32 v44, 0xc2, v235
	v_pk_add_f32 v[88:89], v[94:95], v[54:55]
	v_sub_f32_e32 v55, v100, v65
	v_sub_f32_e32 v54, v100, v64
	v_cndmask_b32_e32 v37, v222, v37, vcc
	v_cmp_le_i32_e32 vcc, v44, v236
	v_pk_add_f32 v[66:67], v[80:81], v[54:55]
	v_or_b32_e32 v44, 0xc3, v235
	v_cndmask_b32_e32 v54, v222, v38, vcc
	v_or_b32_e32 v38, 0xe2, v235
	v_cmp_le_i32_e32 vcc, v38, v236
	v_sub_f32_e32 v57, v100, v57
	v_sub_f32_e32 v56, v100, v56
	v_cndmask_b32_e32 v38, v222, v46, vcc
	v_cmp_le_i32_e32 vcc, v44, v236
	v_sub_f32_e32 v43, v100, v43
	v_sub_f32_e32 v42, v100, v42
	v_cndmask_b32_e32 v55, v222, v39, vcc
	v_or_b32_e32 v39, 0xe3, v235
	v_cmp_le_i32_e32 vcc, v39, v236
	v_or_b32_e32 v44, 0xc8, v235
	v_pk_add_f32 v[42:43], v[90:91], v[42:43]
	v_pk_add_f32 v[90:91], v[96:97], v[56:57]
	v_sub_f32_e32 v57, v100, v63
	v_sub_f32_e32 v56, v100, v62
	v_cndmask_b32_e32 v39, v222, v47, vcc
	v_cmp_le_i32_e32 vcc, v44, v236
	v_sub_f32_e32 v49, v100, v49
	v_sub_f32_e32 v48, v100, v48
	v_pk_add_f32 v[64:65], v[78:79], v[56:57]
	v_cndmask_b32_e32 v56, v222, v40, vcc
	v_or_b32_e32 v40, 0xe8, v235
	v_pk_add_f32 v[48:49], v[72:73], v[48:49]
	v_cmp_le_i32_e32 vcc, v40, v236
	v_or_b32_e32 v44, 0xc9, v235
	v_sub_f32_e32 v59, v100, v59
	v_cndmask_b32_e32 v40, v222, v48, vcc
	v_cmp_le_i32_e32 vcc, v44, v236
	v_sub_f32_e32 v58, v100, v58
	v_or_b32_e32 v44, 0xca, v235
	v_cndmask_b32_e32 v57, v222, v41, vcc
	v_or_b32_e32 v41, 0xe9, v235
	v_cmp_le_i32_e32 vcc, v41, v236
	v_pk_add_f32 v[92:93], v[98:99], v[58:59]
	v_sub_f32_e32 v59, v100, v61
	v_sub_f32_e32 v58, v100, v60
	v_cndmask_b32_e32 v41, v222, v49, vcc
	v_cmp_le_i32_e32 vcc, v44, v236
	v_sub_f32_e32 v51, v100, v51
	v_sub_f32_e32 v50, v100, v50
	v_pk_add_f32 v[62:63], v[76:77], v[58:59]
	v_cndmask_b32_e32 v58, v222, v42, vcc
	v_or_b32_e32 v42, 0xea, v235
	v_pk_add_f32 v[50:51], v[74:75], v[50:51]
	v_cmp_le_i32_e32 vcc, v42, v236
	v_or_b32_e32 v44, 0xcb, v235
	v_or_b32_e32 v45, 0xd1, v235
	v_cndmask_b32_e32 v42, v222, v50, vcc
	v_cmp_le_i32_e32 vcc, v44, v236
	v_or_b32_e32 v44, 0xd0, v235
	v_or_b32_e32 v46, 0xd2, v235
	v_cndmask_b32_e32 v59, v222, v43, vcc
	v_or_b32_e32 v43, 0xeb, v235
	v_cmp_le_i32_e32 vcc, v43, v236
	v_or_b32_e32 v47, 0xd3, v235
	v_or_b32_e32 v48, 0xd8, v235
	v_cndmask_b32_e32 v43, v222, v51, vcc
	v_cmp_le_i32_e32 vcc, v44, v236
	v_or_b32_e32 v44, 0xf0, v235
	v_or_b32_e32 v49, 0xd9, v235
	v_cndmask_b32_e32 v60, v222, v86, vcc
	v_cmp_le_i32_e32 vcc, v44, v236
	v_max_f32_e32 v68, v52, v53
	v_or_b32_e32 v50, 0xda, v235
	v_cndmask_b32_e32 v44, v222, v62, vcc
	v_cmp_le_i32_e32 vcc, v45, v236
	v_or_b32_e32 v45, 0xf1, v235
	v_max3_f32 v69, v54, v55, v37
	v_cndmask_b32_e32 v61, v222, v87, vcc
	v_cmp_le_i32_e32 vcc, v45, v236
	v_max3_f32 v68, v68, v36, v38
	v_max3_f32 v68, v68, v39, v56
	v_cndmask_b32_e32 v45, v222, v63, vcc
	v_cmp_le_i32_e32 vcc, v46, v236
	v_or_b32_e32 v46, 0xf2, v235
	v_max3_f32 v69, v69, v58, v59
	v_cndmask_b32_e32 v62, v222, v88, vcc
	v_cmp_le_i32_e32 vcc, v46, v236
	v_or_b32_e32 v51, 0xdb, v235
	v_max3_f32 v68, v68, v57, v40
	v_cndmask_b32_e32 v46, v222, v64, vcc
	v_cmp_le_i32_e32 vcc, v47, v236
	v_or_b32_e32 v47, 0xf3, v235
	v_max3_f32 v69, v69, v42, v43
	v_cndmask_b32_e32 v63, v222, v89, vcc
	v_cmp_le_i32_e32 vcc, v47, v236
	v_max3_f32 v68, v68, v41, v60
	v_max3_f32 v69, v69, v62, v63
	v_cndmask_b32_e32 v47, v222, v65, vcc
	v_cmp_le_i32_e32 vcc, v48, v236
	v_or_b32_e32 v48, 0xf8, v235
	v_max3_f32 v68, v68, v61, v44
	v_cndmask_b32_e32 v64, v222, v90, vcc
	v_cmp_le_i32_e32 vcc, v48, v236
	v_max3_f32 v69, v69, v46, v47
	v_max3_f32 v68, v68, v45, v64
	v_cndmask_b32_e32 v48, v222, v66, vcc
	v_cmp_le_i32_e32 vcc, v49, v236
	v_or_b32_e32 v49, 0xf9, v235
	v_add_f32_e32 v2, v241, v2
	v_cndmask_b32_e32 v65, v222, v91, vcc
	v_cmp_le_i32_e32 vcc, v49, v236
	v_max3_f32 v68, v68, v65, v48
	s_nop 0
	v_cndmask_b32_e32 v49, v222, v67, vcc
	v_cmp_le_i32_e32 vcc, v50, v236
	v_or_b32_e32 v50, 0xfa, v235
	s_nop 0
	v_cndmask_b32_e32 v66, v222, v92, vcc
	v_cmp_le_i32_e32 vcc, v50, v236
	s_nop 1
	v_cndmask_b32_e32 v50, v222, v70, vcc
	v_cmp_le_i32_e32 vcc, v51, v236
	v_or_b32_e32 v51, 0xfb, v235
	s_nop 0
	v_cndmask_b32_e32 v67, v222, v93, vcc
	v_cmp_le_i32_e32 vcc, v51, v236
	v_max3_f32 v69, v69, v66, v67
	s_nop 0
	v_cndmask_b32_e32 v51, v222, v71, vcc
	v_max3_f32 v69, v69, v50, v51
	v_max3_f32 v68, v68, v49, v69
	v_mov_b32_e32 v69, v68
	s_nop 1
	v_permlane32_swap_b32_e32 v68, v69
	v_max_f32_e32 v69, v69, v69
	v_max_f32_e32 v68, v68, v68
	v_max_f32_e32 v68, v68, v69
	v_cmp_lt_f32_e32 vcc, s94, v68
	s_cmp_lg_u64 vcc, 0
	s_cselect_b64 s[4:5], -1, 0
	s_cbranch_vccnz .LBB0_1024

; #define SBAR() __builtin_amdgcn_sched_barrier(0)
;   #define PKW(P,B) cvtpk_s(P[B],P[B+1])
;   #define PKW(P,B) cvtpk_s(P[B],P[B+1])
; __device__ __forceinline__ void pv(f32x16*o,int vb,bf16x8 pa0,bf16x8 pa1,bf16x8 pa2,bf16x8 pa3){
;   #pragma unroll
;   for(int d0=0;d0<2;++d0){s16x4 lo[4],hi[4];
;     #pragma unroll
;     for(int ks=0;ks<4;++ks){
;       asm volatile("ds_read_b64_tr_b16 %0,%1 offset:%c2":"=&v"(lo[ks]):"v"(vb),"i"(d0*4096+ks*1024):"memory");
;       asm volatile("ds_read_b64_tr_b16 %0,%1 offset:%c2":"=&v"(hi[ks]):"v"(vb),"i"(d0*4096+ks*1024+512):"memory");}
;     asm volatile("s_waitcnt lgkmcnt(0)":::"memory");SBAR();
;     ...
;     o[d0]=__builtin_amdgcn_mfma_f32_32x32x16_bf16(pa0,PK(0),o[d0],0,0,0);
;     o[d0]=__builtin_amdgcn_mfma_f32_32x32x16_bf16(pa1,PK(1),o[d0],0,0,0);
;     o[d0]=__builtin_amdgcn_mfma_f32_32x32x16_bf16(pa2,PK(2),o[d0],0,0,0);
;     o[d0]=__builtin_amdgcn_mfma_f32_32x32x16_bf16(pa3,PK(3),o[d0],0,0,0);
;     ...
;   }
; }
;     ...
;   { float sacc=pB0[0]+pB0[1]; _Pragma("unroll") for(int r=2;r<16;++r)sacc+=pB0[r]; _Pragma("unroll") for(int r=0;r<16;++r)sacc+=pB1[r]; l_reg+=sacc;
;     pw0=(u32x4){PKW(pB0,0),PKW(pB0,2),PKW(pB0,4),PKW(pB0,6)};pw1=(u32x4){PKW(pB0,8),PKW(pB0,10),PKW(pB0,12),PKW(pB0,14)};pw2=(u32x4){PKW(pB1,0),PKW(pB1,2),PKW(pB1,4),PKW(pB1,6)};pw3=(u32x4){PKW(pB1,8),PKW(pB1,10),PKW(pB1,12),PKW(pB1,14)};
;     SBAR(); pv(o,vb0+sl_cur,PAF(0),PAF(1),PAF(2),PAF(3)); }
;     ...
;   {auto rr=__builtin_amdgcn_permlane32_swap(__float_as_uint(l_reg),__float_as_uint(l_reg),false,false);l_reg=__uint_as_float(rr[0])+__uint_as_float(rr[1]);}
;   if(hi==0)wsf[32+r32]=l_reg;asm volatile("s_waitcnt lgkmcnt(0)":::"memory");
.LBB0_972:
	v_pk_add_f32 v[254:255], v[52:53], v[54:55]
	v_pk_add_f32 v[254:255], v[254:255], v[56:57]
	v_pk_add_f32 v[254:255], v[254:255], v[58:59]
	v_pk_add_f32 v[254:255], v[254:255], v[60:61]
	v_pk_add_f32 v[254:255], v[254:255], v[62:63]
	v_pk_add_f32 v[254:255], v[254:255], v[64:65]
	v_pk_add_f32 v[254:255], v[254:255], v[66:67]
	v_pk_add_f32 v[254:255], v[254:255], v[36:37]
	v_pk_add_f32 v[254:255], v[254:255], v[38:39]
	v_pk_add_f32 v[254:255], v[254:255], v[40:41]
	v_pk_add_f32 v[254:255], v[254:255], v[42:43]
	v_pk_add_f32 v[254:255], v[254:255], v[44:45]
	v_pk_add_f32 v[254:255], v[254:255], v[46:47]
	v_pk_add_f32 v[254:255], v[254:255], v[48:49]
	s_cmp_lg_u32 0, -1
	v_pk_add_f32 v[254:255], v[254:255], v[50:51]
	s_cselect_b32 s4, 0, 0
	v_add_f32_e32 v69, v254, v255
	s_addk_i32 s4, 0x6000
	v_add_f32_e32 v2, v2, v69
	v_cvt_pk_bf16_f32 v36, v36, v37
	v_add3_u32 v68, v234, s4, v231
	v_cvt_pk_bf16_f32 v52, v52, v53
	v_cvt_pk_bf16_f32 v53, v54, v55
	v_cvt_pk_bf16_f32 v54, v56, v57
	v_cvt_pk_bf16_f32 v55, v58, v59
	v_cvt_pk_bf16_f32 v56, v60, v61
	v_cvt_pk_bf16_f32 v57, v62, v63
	v_cvt_pk_bf16_f32 v58, v64, v65
	v_cvt_pk_bf16_f32 v59, v66, v67
	v_cvt_pk_bf16_f32 v37, v38, v39
	v_cvt_pk_bf16_f32 v38, v40, v41
	v_cvt_pk_bf16_f32 v39, v42, v43
	v_cvt_pk_bf16_f32 v40, v44, v45
	v_cvt_pk_bf16_f32 v41, v46, v47
	v_cvt_pk_bf16_f32 v42, v48, v49
	v_cvt_pk_bf16_f32 v43, v50, v51
	v_add3_u32 v68, v68, v232, s61
	ds_read_b64_tr_b16 v[44:45],v68 offset:0
	ds_read_b64_tr_b16 v[46:47],v68 offset:512
	ds_read_b64_tr_b16 v[48:49],v68 offset:1024
	ds_read_b64_tr_b16 v[50:51],v68 offset:1536
	ds_read_b64_tr_b16 v[60:61],v68 offset:2048
	ds_read_b64_tr_b16 v[62:63],v68 offset:2560
	ds_read_b64_tr_b16 v[64:65],v68 offset:3072
	ds_read_b64_tr_b16 v[66:67],v68 offset:3584
	s_waitcnt lgkmcnt(0)
	s_nop 0
	v_mfma_f32_32x32x16_bf16 v[20:35], v[52:55], v[44:47], v[20:35]
	ds_read_b64_tr_b16 v[44:45],v68 offset:4096
	ds_read_b64_tr_b16 v[46:47],v68 offset:4608
	v_mfma_f32_32x32x16_bf16 v[20:35], v[56:59], v[48:51], v[20:35]
	ds_read_b64_tr_b16 v[48:49],v68 offset:5120
	ds_read_b64_tr_b16 v[50:51],v68 offset:5632
	v_mfma_f32_32x32x16_bf16 v[20:35], v[36:39], v[60:63], v[20:35]
	ds_read_b64_tr_b16 v[60:61],v68 offset:6144
	ds_read_b64_tr_b16 v[62:63],v68 offset:6656
	v_mfma_f32_32x32x16_bf16 v[20:35], v[40:43], v[64:67], v[20:35]
	ds_read_b64_tr_b16 v[64:65],v68 offset:7168
	ds_read_b64_tr_b16 v[66:67],v68 offset:7680
	s_waitcnt lgkmcnt(0)
	v_mfma_f32_32x32x16_bf16 v[4:19], v[52:55], v[44:47], v[4:19]
	v_cmp_gt_u32_e32 vcc, 32, v227
	v_mfma_f32_32x32x16_bf16 v[4:19], v[56:59], v[48:51], v[4:19]
	v_mfma_f32_32x32x16_bf16 v[4:19], v[36:39], v[60:63], v[4:19]
	v_mov_b32_e32 v36, v2
	s_nop 1
	v_permlane32_swap_b32_e32 v2, v36
	v_mfma_f32_32x32x16_bf16 v[4:19], v[40:43], v[64:67], v[4:19]
	s_and_saveexec_b64 s[4:5], vcc
	s_cbranch_execz .LBB0_930
	v_lshl_add_u32 v37, v229, 2, s56
	v_add_f32_e32 v2, v2, v36
	ds_write_b32 v37, v2 offset:49280
	s_branch .LBB0_930

.LBB0_976:
	v_add_u32_e32 v2, s7, v240
	ds_read_b64_tr_b16 v[176:177], v2 offset:24576
	ds_read_b64_tr_b16 v[178:179], v2 offset:25088
	s_waitcnt lgkmcnt(3)
	v_mfma_f32_32x32x16_bf16 v[84:99], v[160:163], v[116:119], 0
	v_pk_add_f32 v[254:255], v[52:53], v[54:55]
	v_pk_add_f32 v[254:255], v[254:255], v[56:57]
	v_cvt_pk_bf16_f32 v128, v52, v53
	v_cvt_pk_bf16_f32 v129, v54, v55
	ds_read_b64_tr_b16 v[160:161], v2 offset:28672
	ds_read_b64_tr_b16 v[162:163], v2 offset:29184
	v_pk_add_f32 v[254:255], v[254:255], v[58:59]
	s_waitcnt lgkmcnt(4)
	v_mfma_f32_32x32x16_bf16 v[68:83], v[152:155], v[116:119], 0
	v_pk_add_f32 v[254:255], v[254:255], v[60:61]
	v_cvt_pk_bf16_f32 v130, v56, v57
	v_cvt_pk_bf16_f32 v131, v58, v59
	ds_read_b64_tr_b16 v[164:165], v2 offset:25600
	ds_read_b64_tr_b16 v[166:167], v2 offset:26112
	s_waitcnt lgkmcnt(11)
	v_mfma_f32_32x32x16_bf16 v[84:99], v[156:159], v[108:111], v[84:99]
	v_pk_add_f32 v[254:255], v[254:255], v[62:63]
	v_pk_add_f32 v[254:255], v[254:255], v[64:65]
	v_cvt_pk_bf16_f32 v124, v60, v61
	v_cvt_pk_bf16_f32 v125, v62, v63
	ds_read_b64_tr_b16 v[168:169], v2 offset:29696
	ds_read_b64_tr_b16 v[170:171], v2 offset:30208
	s_waitcnt lgkmcnt(12)
	v_mfma_f32_32x32x16_bf16 v[68:83], v[148:151], v[108:111], v[68:83]
	v_pk_add_f32 v[254:255], v[254:255], v[66:67]
	v_pk_add_f32 v[254:255], v[254:255], v[36:37]
	v_cvt_pk_bf16_f32 v126, v64, v65
	v_cvt_pk_bf16_f32 v127, v66, v67
	ds_read_b64_tr_b16 v[172:173], v2 offset:26624
	ds_read_b64_tr_b16 v[174:175], v2 offset:27136
	s_waitcnt lgkmcnt(13)
	v_mfma_f32_32x32x16_bf16 v[84:99], v[144:147], v[104:107], v[84:99]
	v_pk_add_f32 v[254:255], v[254:255], v[38:39]
	v_pk_add_f32 v[254:255], v[254:255], v[40:41]
	v_cvt_pk_bf16_f32 v120, v36, v37
	v_cvt_pk_bf16_f32 v121, v38, v39
	ds_read_b64_tr_b16 v[180:181], v2 offset:30720
	ds_read_b64_tr_b16 v[182:183], v2 offset:31232
	s_waitcnt lgkmcnt(14)
	v_mfma_f32_32x32x16_bf16 v[68:83], v[140:143], v[104:107], v[68:83]
	v_pk_add_f32 v[254:255], v[254:255], v[42:43]
	v_pk_add_f32 v[254:255], v[254:255], v[44:45]
	v_cvt_pk_bf16_f32 v122, v40, v41
	v_cvt_pk_bf16_f32 v123, v42, v43
	ds_read_b64_tr_b16 v[184:185], v2 offset:27648
	ds_read_b64_tr_b16 v[186:187], v2 offset:28160
	s_waitcnt lgkmcnt(14)
	v_mfma_f32_32x32x16_bf16 v[84:99], v[136:139], v[100:103], v[84:99]
	v_pk_add_f32 v[254:255], v[254:255], v[46:47]
	v_pk_add_f32 v[254:255], v[254:255], v[48:49]
	v_cvt_pk_bf16_f32 v112, v44, v45
	v_cvt_pk_bf16_f32 v113, v46, v47
	ds_read_b64_tr_b16 v[188:189], v2 offset:31744
	ds_read_b64_tr_b16 v[190:191], v2 offset:32256
	v_mfma_f32_32x32x16_bf16 v[68:83], v[132:135], v[100:103], v[68:83]
	v_pk_add_f32 v[254:255], v[254:255], v[50:51]
	v_add_f32_e32 v2, v254, v255
	v_add_f32_e32 v2, 0, v2
	v_cvt_pk_bf16_f32 v114, v48, v49
	v_cvt_pk_bf16_f32 v115, v50, v51
	s_add_i32 s6, s34, 1
	s_cmp_ge_i32 s6, s60
	s_cselect_b64 s[26:27], -1, 0
	s_and_b64 vcc, exec, s[26:27]
	s_cbranch_vccnz .LBB0_978
	v_lshl_add_u64 v[36:37], v[196:197], 0, s[18:19]
	s_mov_b64 s[6:7], 0x13060000
	s_add_i32 s28, s61, s58
	v_lshl_add_u64 v[36:37], v[36:37], 0, s[6:7]
	s_mov_b32 s6, m0
	s_mov_b32 m0, s28
	s_nop 0
	global_load_lds_dwordx4 v[36:37], off
	s_mov_b32 m0, s6

.LBB0_985:
	v_add_u32_e32 v166, s61, v240
	ds_read_b64_tr_b16 v[192:193], v166 offset:24576
	ds_read_b64_tr_b16 v[194:195], v166 offset:25088
	s_waitcnt lgkmcnt(9)
	v_mfma_f32_32x32x16_bf16 v[84:99], v[160:163], v[116:119], 0
	v_pk_add_f32 v[254:255], v[52:53], v[54:55]
	v_pk_add_f32 v[254:255], v[254:255], v[56:57]
	v_cvt_pk_bf16_f32 v128, v52, v53
	v_cvt_pk_bf16_f32 v129, v54, v55
	ds_read_b64_tr_b16 v[188:189], v166 offset:28672
	ds_read_b64_tr_b16 v[190:191], v166 offset:29184
	v_pk_add_f32 v[254:255], v[254:255], v[58:59]
	s_waitcnt lgkmcnt(10)
	v_mfma_f32_32x32x16_bf16 v[68:83], v[152:155], v[116:119], 0
	v_pk_add_f32 v[254:255], v[254:255], v[60:61]
	v_cvt_pk_bf16_f32 v130, v56, v57
	v_cvt_pk_bf16_f32 v131, v58, v59
	ds_read_b64_tr_b16 v[184:185], v166 offset:25600
	ds_read_b64_tr_b16 v[186:187], v166 offset:26112
	s_waitcnt lgkmcnt(11)
	v_mfma_f32_32x32x16_bf16 v[84:99], v[156:159], v[108:111], v[84:99]
	v_pk_add_f32 v[254:255], v[254:255], v[62:63]
	v_pk_add_f32 v[254:255], v[254:255], v[64:65]
	v_cvt_pk_bf16_f32 v124, v60, v61
	v_cvt_pk_bf16_f32 v125, v62, v63
	ds_read_b64_tr_b16 v[180:181], v166 offset:29696
	ds_read_b64_tr_b16 v[182:183], v166 offset:30208
	s_waitcnt lgkmcnt(12)
	v_mfma_f32_32x32x16_bf16 v[68:83], v[148:151], v[108:111], v[68:83]
	v_pk_add_f32 v[254:255], v[254:255], v[66:67]
	v_pk_add_f32 v[254:255], v[254:255], v[36:37]
	v_cvt_pk_bf16_f32 v126, v64, v65
	v_cvt_pk_bf16_f32 v127, v66, v67
	ds_read_b64_tr_b16 v[176:177], v166 offset:26624
	ds_read_b64_tr_b16 v[178:179], v166 offset:27136
	s_waitcnt lgkmcnt(13)
	v_mfma_f32_32x32x16_bf16 v[84:99], v[144:147], v[104:107], v[84:99]
	v_pk_add_f32 v[254:255], v[254:255], v[38:39]
	v_pk_add_f32 v[254:255], v[254:255], v[40:41]
	v_cvt_pk_bf16_f32 v120, v36, v37
	v_cvt_pk_bf16_f32 v121, v38, v39
	ds_read_b64_tr_b16 v[172:173], v166 offset:30720
	ds_read_b64_tr_b16 v[174:175], v166 offset:31232
	s_waitcnt lgkmcnt(14)
	v_mfma_f32_32x32x16_bf16 v[68:83], v[140:143], v[104:107], v[68:83]
	v_pk_add_f32 v[254:255], v[254:255], v[42:43]
	v_pk_add_f32 v[254:255], v[254:255], v[44:45]
	v_cvt_pk_bf16_f32 v122, v40, v41
	v_cvt_pk_bf16_f32 v123, v42, v43
	ds_read_b64_tr_b16 v[168:169], v166 offset:27648
	ds_read_b64_tr_b16 v[170:171], v166 offset:28160
	s_waitcnt lgkmcnt(14)
	v_mfma_f32_32x32x16_bf16 v[84:99], v[136:139], v[100:103], v[84:99]
	v_pk_add_f32 v[254:255], v[254:255], v[46:47]
	v_pk_add_f32 v[254:255], v[254:255], v[48:49]
	v_cvt_pk_bf16_f32 v112, v44, v45
	v_cvt_pk_bf16_f32 v113, v46, v47
	ds_read_b64_tr_b16 v[164:165], v166 offset:31744
	ds_read_b64_tr_b16 v[166:167], v166 offset:32256
	v_mfma_f32_32x32x16_bf16 v[68:83], v[132:135], v[100:103], v[68:83]
	v_pk_add_f32 v[254:255], v[254:255], v[50:51]
	v_add_f32_e32 v36, v254, v255
	v_add_f32_e32 v241, 0, v36
	v_cvt_pk_bf16_f32 v114, v48, v49
	v_cvt_pk_bf16_f32 v115, v50, v51
	s_add_i32 s64, s34, 2
	s_cmp_ge_i32 s64, s60
	s_cselect_b64 s[28:29], -1, 0
	s_and_b64 vcc, exec, s[28:29]
	s_cbranch_vccnz .LBB0_987
	v_lshl_add_u64 v[36:37], v[196:197], 0, s[18:19]
	s_mov_b64 s[30:31], 0x13080000
	s_add_i32 s6, s38, s58
	v_lshl_add_u64 v[36:37], v[36:37], 0, s[30:31]
	s_mov_b32 s7, m0
	s_mov_b32 m0, s6
	s_nop 0
	global_load_lds_dwordx4 v[36:37], off
	s_mov_b32 m0, s7

.LBB0_1425:
	v_add_u32_e32 v170, s72, v239
	ds_read_b64_tr_b16 v[166:167], v170 offset:24576
	ds_read_b64_tr_b16 v[168:169], v170 offset:25088
	v_pk_add_f32 v[254:255], v[52:53], v[54:55]
	v_cvt_pk_bf16_f32 v52, v52, v53
	v_pk_add_f32 v[254:255], v[254:255], v[56:57]
	v_cndmask_b32_e64 v130, 0, v52, s[92:93]
	v_cvt_pk_bf16_f32 v52, v54, v55
	v_cndmask_b32_e64 v131, 0, v52, s[92:93]
	s_waitcnt lgkmcnt(9)
	v_mfma_f32_32x32x16_bf16 v[68:83], v[162:165], v[126:129], 0
	ds_read_b64_tr_b16 v[162:163], v170 offset:28672
	ds_read_b64_tr_b16 v[164:165], v170 offset:29184
	v_pk_add_f32 v[254:255], v[254:255], v[58:59]
	v_cvt_pk_bf16_f32 v53, v56, v57
	v_pk_add_f32 v[254:255], v[254:255], v[60:61]
	v_cndmask_b32_e64 v132, 0, v53, s[92:93]
	v_cvt_pk_bf16_f32 v53, v58, v59
	v_cndmask_b32_e64 v133, 0, v53, s[92:93]
	s_waitcnt lgkmcnt(10)
	v_mfma_f32_32x32x16_bf16 v[84:99], v[154:157], v[126:129], 0
	ds_read_b64_tr_b16 v[154:155], v170 offset:25600
	ds_read_b64_tr_b16 v[156:157], v170 offset:26112
	v_pk_add_f32 v[254:255], v[254:255], v[62:63]
	v_cvt_pk_bf16_f32 v53, v60, v61
	v_pk_add_f32 v[254:255], v[254:255], v[64:65]
	v_cndmask_b32_e64 v108, 0, v53, s[92:93]
	v_cvt_pk_bf16_f32 v53, v62, v63
	v_cndmask_b32_e64 v109, 0, v53, s[92:93]
	s_waitcnt lgkmcnt(11)
	v_mfma_f32_32x32x16_bf16 v[68:83], v[158:161], v[122:125], v[68:83]
	ds_read_b64_tr_b16 v[158:159], v170 offset:29696
	ds_read_b64_tr_b16 v[160:161], v170 offset:30208
	v_pk_add_f32 v[254:255], v[254:255], v[66:67]
	v_cvt_pk_bf16_f32 v53, v64, v65
	v_pk_add_f32 v[254:255], v[254:255], v[36:37]
	v_cndmask_b32_e64 v110, 0, v53, s[92:93]
	v_cvt_pk_bf16_f32 v53, v66, v67
	v_cndmask_b32_e64 v111, 0, v53, s[92:93]
	s_waitcnt lgkmcnt(12)
	v_mfma_f32_32x32x16_bf16 v[84:99], v[150:153], v[122:125], v[84:99]
	ds_read_b64_tr_b16 v[150:151], v170 offset:26624
	ds_read_b64_tr_b16 v[152:153], v170 offset:27136
	v_pk_add_f32 v[254:255], v[254:255], v[38:39]
	v_cvt_pk_bf16_f32 v36, v36, v37
	v_pk_add_f32 v[254:255], v[254:255], v[40:41]
	v_cndmask_b32_e64 v104, 0, v36, s[92:93]
	v_cvt_pk_bf16_f32 v36, v38, v39
	v_cndmask_b32_e64 v105, 0, v36, s[92:93]
	s_waitcnt lgkmcnt(13)
	v_mfma_f32_32x32x16_bf16 v[68:83], v[146:149], v[118:121], v[68:83]
	ds_read_b64_tr_b16 v[146:147], v170 offset:30720
	ds_read_b64_tr_b16 v[148:149], v170 offset:31232
	v_pk_add_f32 v[254:255], v[254:255], v[42:43]
	v_cvt_pk_bf16_f32 v37, v40, v41
	v_pk_add_f32 v[254:255], v[254:255], v[44:45]
	v_cndmask_b32_e64 v106, 0, v37, s[92:93]
	v_cvt_pk_bf16_f32 v37, v42, v43
	v_cndmask_b32_e64 v107, 0, v37, s[92:93]
	s_waitcnt lgkmcnt(14)
	v_mfma_f32_32x32x16_bf16 v[84:99], v[142:145], v[118:121], v[84:99]
	ds_read_b64_tr_b16 v[142:143], v170 offset:27648
	ds_read_b64_tr_b16 v[144:145], v170 offset:28160
	v_pk_add_f32 v[254:255], v[254:255], v[46:47]
	v_cvt_pk_bf16_f32 v37, v44, v45
	v_pk_add_f32 v[254:255], v[254:255], v[48:49]
	v_cndmask_b32_e64 v100, 0, v37, s[92:93]
	v_cvt_pk_bf16_f32 v37, v46, v47
	v_cndmask_b32_e64 v101, 0, v37, s[92:93]
	s_waitcnt lgkmcnt(14)
	v_mfma_f32_32x32x16_bf16 v[68:83], v[138:141], v[114:117], v[68:83]
	ds_read_b64_tr_b16 v[138:139], v170 offset:31744
	ds_read_b64_tr_b16 v[140:141], v170 offset:32256
	v_pk_add_f32 v[254:255], v[254:255], v[50:51]
	v_add_f32_e32 v36, v254, v255
	v_mfma_f32_32x32x16_bf16 v[84:99], v[134:137], v[114:117], v[84:99]
	v_add_f32_e32 v134, 0, v36
	v_cvt_pk_bf16_f32 v36, v48, v49
	v_cndmask_b32_e64 v102, 0, v36, s[92:93]
	v_cvt_pk_bf16_f32 v36, v50, v51
	v_cndmask_b32_e64 v103, 0, v36, s[92:93]
	v_mov_b32_e32 v36, s85
	ds_read_b32 v37, v36 offset:12
	v_pk_add_f32 v[52:53], v[68:69], v[2:3] op_sel_hi:[1,0] neg_lo:[0,1] neg_hi:[0,1]
	v_pk_add_f32 v[54:55], v[70:71], v[2:3] op_sel_hi:[1,0] neg_lo:[0,1] neg_hi:[0,1]
	s_nop 2
	v_pk_add_f32 v[38:39], v[86:87], v[2:3] op_sel_hi:[1,0] neg_lo:[0,1] neg_hi:[0,1]
	v_pk_add_f32 v[56:57], v[72:73], v[2:3] op_sel_hi:[1,0] neg_lo:[0,1] neg_hi:[0,1]
	s_waitcnt lgkmcnt(0)
	v_readfirstlane_b32 s4, v37
	s_lshl_b32 s4, s4, 13
	s_and_b32 s4, s4, 0x7e000
	s_add_u32 s72, s77, s4
	s_addc_u32 s73, s78, 0
	s_add_i32 s4, s91, s95
	s_mov_b32 s76, m0
	s_mov_b32 m0, s4
	s_nop 0
	global_load_lds_dwordx4 v236, s[72:73]
	s_mov_b32 m0, s76
	ds_read_b32 v37, v36 offset:4
	v_pk_add_f32 v[40:41], v[88:89], v[2:3] op_sel_hi:[1,0] neg_lo:[0,1] neg_hi:[0,1]
	v_pk_add_f32 v[58:59], v[74:75], v[2:3] op_sel_hi:[1,0] neg_lo:[0,1] neg_hi:[0,1]
	v_pk_add_f32 v[42:43], v[90:91], v[2:3] op_sel_hi:[1,0] neg_lo:[0,1] neg_hi:[0,1]
	v_pk_add_f32 v[60:61], v[76:77], v[2:3] op_sel_hi:[1,0] neg_lo:[0,1] neg_hi:[0,1]
	s_waitcnt lgkmcnt(0)
	v_readfirstlane_b32 s4, v37
	s_lshl_b32 s4, s4, 13
	s_and_b32 s4, s4, 0x7e000
	s_add_u32 s72, s79, s4
	s_addc_u32 s73, s88, 0
	s_add_i32 s4, s90, s75
	s_mov_b32 s76, m0
	s_mov_b32 m0, s4
	s_nop 0
	global_load_lds_dwordx4 v237, s[72:73]
	s_mov_b32 m0, s76
	ds_read_b32 v36, v36
	v_pk_add_f32 v[44:45], v[92:93], v[2:3] op_sel_hi:[1,0] neg_lo:[0,1] neg_hi:[0,1]
	v_pk_add_f32 v[62:63], v[78:79], v[2:3] op_sel_hi:[1,0] neg_lo:[0,1] neg_hi:[0,1]
	v_pk_add_f32 v[46:47], v[94:95], v[2:3] op_sel_hi:[1,0] neg_lo:[0,1] neg_hi:[0,1]
	v_pk_add_f32 v[64:65], v[80:81], v[2:3] op_sel_hi:[1,0] neg_lo:[0,1] neg_hi:[0,1]
	s_waitcnt lgkmcnt(0)
	v_readfirstlane_b32 s4, v36
	s_and_b32 s72, s4, 63
	s_sub_i32 s73, s94, s72
	v_pk_add_f32 v[36:37], v[84:85], v[2:3] op_sel_hi:[1,0] neg_lo:[0,1] neg_hi:[0,1]
	v_pk_add_f32 v[48:49], v[96:97], v[2:3] op_sel_hi:[1,0] neg_lo:[0,1] neg_hi:[0,1]
	v_pk_add_f32 v[66:67], v[82:83], v[2:3] op_sel_hi:[1,0] neg_lo:[0,1] neg_hi:[0,1]
	v_pk_add_f32 v[50:51], v[98:99], v[2:3] op_sel_hi:[1,0] neg_lo:[0,1] neg_hi:[0,1]
	s_cmp_gt_i32 s73, 2
	s_cbranch_scc1 .LBB0_1427
	v_lshl_add_u32 v99, s73, 8, v183
	ds_read_b32 v68, v99 offset:256
	ds_read_b32 v70, v99 offset:128
	ds_read_b32 v69, v99 offset:252
	ds_read_b32 v71, v99 offset:124
	ds_read_b32 v72, v99 offset:248
	ds_read_b32 v74, v99 offset:120
	ds_read_b32 v73, v99 offset:244
	ds_read_b32 v75, v99 offset:116
	ds_read_b32 v76, v99 offset:224
	ds_read_b32 v78, v99 offset:96
	ds_read_b32 v77, v99 offset:220
	ds_read_b32 v79, v99 offset:92
	ds_read_b32 v80, v99 offset:216
	ds_read_b32 v82, v99 offset:88
	ds_read_b32 v81, v99 offset:212
	ds_read_b32 v83, v99 offset:84
	ds_read_b32 v84, v99 offset:192
	ds_read_b32 v86, v99 offset:64
	ds_read_b32 v85, v99 offset:188
	ds_read_b32 v87, v99 offset:60
	ds_read_b32 v88, v99 offset:184
	ds_read_b32 v90, v99 offset:56
	ds_read_b32 v89, v99 offset:180
	ds_read_b32 v91, v99 offset:52
	ds_read_b32 v92, v99 offset:160
	ds_read_b32 v94, v99 offset:32
	ds_read_b32 v93, v99 offset:156
	ds_read_b32 v95, v99 offset:28
	ds_read_b32 v96, v99 offset:152
	ds_read_b32 v98, v99 offset:24
	ds_read_b32 v97, v99 offset:148
	ds_read_b32 v99, v99 offset:20
	s_waitcnt lgkmcnt(14)
	v_pk_add_f32 v[52:53], v[52:53], v[68:69]
	v_pk_add_f32 v[54:55], v[54:55], v[72:73]
	v_pk_add_f32 v[56:57], v[56:57], v[76:77]
	v_pk_add_f32 v[58:59], v[58:59], v[80:81]
	s_waitcnt lgkmcnt(13)
	v_pk_add_f32 v[60:61], v[60:61], v[84:85]
	s_waitcnt lgkmcnt(9)
	v_pk_add_f32 v[62:63], v[62:63], v[88:89]
	s_waitcnt lgkmcnt(5)
	v_pk_add_f32 v[64:65], v[64:65], v[92:93]
	s_waitcnt lgkmcnt(1)
	v_pk_add_f32 v[66:67], v[66:67], v[96:97]
	v_pk_add_f32 v[36:37], v[36:37], v[70:71]
	v_pk_add_f32 v[38:39], v[38:39], v[74:75]
	v_pk_add_f32 v[40:41], v[40:41], v[78:79]
	v_pk_add_f32 v[42:43], v[42:43], v[82:83]
	v_pk_add_f32 v[44:45], v[44:45], v[86:87]
	v_pk_add_f32 v[46:47], v[46:47], v[90:91]
	v_pk_add_f32 v[48:49], v[48:49], v[94:95]
	s_waitcnt lgkmcnt(0)
	v_pk_add_f32 v[50:51], v[50:51], v[98:99]

.LBB0_1432:
	s_add_i32 s4, s90, 0x2000
	s_cmpk_lg_i32 s90, 0x4000
	s_cselect_b32 s84, s4, 0
	v_add_u32_e32 v180, s91, v239
	ds_read_b64_tr_b16 v[138:139], v180 offset:24576
	ds_read_b64_tr_b16 v[140:141], v180 offset:25088
	v_pk_add_f32 v[254:255], v[52:53], v[54:55]
	v_cvt_pk_bf16_f32 v52, v52, v53
	v_pk_add_f32 v[254:255], v[254:255], v[56:57]
	v_cndmask_b32_e64 v130, 0, v52, s[72:73]
	v_cvt_pk_bf16_f32 v52, v54, v55
	v_cndmask_b32_e64 v131, 0, v52, s[72:73]
	s_waitcnt lgkmcnt(9)
	v_mfma_f32_32x32x16_bf16 v[68:83], v[68:71], v[126:129], 0
	ds_read_b64_tr_b16 v[142:143], v180 offset:28672
	ds_read_b64_tr_b16 v[144:145], v180 offset:29184
	v_pk_add_f32 v[254:255], v[254:255], v[58:59]
	v_cvt_pk_bf16_f32 v53, v56, v57
	v_pk_add_f32 v[254:255], v[254:255], v[60:61]
	v_cndmask_b32_e64 v132, 0, v53, s[72:73]
	v_cvt_pk_bf16_f32 v53, v58, v59
	v_cndmask_b32_e64 v133, 0, v53, s[72:73]
	s_waitcnt lgkmcnt(10)
	v_mfma_f32_32x32x16_bf16 v[84:99], v[84:87], v[126:129], 0
	ds_read_b64_tr_b16 v[134:135], v180 offset:25600
	ds_read_b64_tr_b16 v[136:137], v180 offset:26112
	v_pk_add_f32 v[254:255], v[254:255], v[62:63]
	v_cvt_pk_bf16_f32 v53, v60, v61
	v_pk_add_f32 v[254:255], v[254:255], v[64:65]
	v_cndmask_b32_e64 v108, 0, v53, s[72:73]
	v_cvt_pk_bf16_f32 v53, v62, v63
	v_cndmask_b32_e64 v109, 0, v53, s[72:73]
	s_waitcnt lgkmcnt(11)
	v_mfma_f32_32x32x16_bf16 v[68:83], v[170:173], v[122:125], v[68:83]
	ds_read_b64_tr_b16 v[146:147], v180 offset:29696
	ds_read_b64_tr_b16 v[148:149], v180 offset:30208
	v_pk_add_f32 v[254:255], v[254:255], v[66:67]
	v_cvt_pk_bf16_f32 v53, v64, v65
	v_pk_add_f32 v[254:255], v[254:255], v[36:37]
	v_cndmask_b32_e64 v110, 0, v53, s[72:73]
	v_cvt_pk_bf16_f32 v53, v66, v67
	v_cndmask_b32_e64 v111, 0, v53, s[72:73]
	s_waitcnt lgkmcnt(12)
	v_mfma_f32_32x32x16_bf16 v[84:99], v[166:169], v[122:125], v[84:99]
	ds_read_b64_tr_b16 v[166:167], v180 offset:26624
	ds_read_b64_tr_b16 v[168:169], v180 offset:27136
	v_pk_add_f32 v[254:255], v[254:255], v[38:39]
	v_cvt_pk_bf16_f32 v36, v36, v37
	v_pk_add_f32 v[254:255], v[254:255], v[40:41]
	v_cndmask_b32_e64 v104, 0, v36, s[72:73]
	v_cvt_pk_bf16_f32 v36, v38, v39
	v_cndmask_b32_e64 v105, 0, v36, s[72:73]
	s_waitcnt lgkmcnt(13)
	v_mfma_f32_32x32x16_bf16 v[68:83], v[162:165], v[118:121], v[68:83]
	ds_read_b64_tr_b16 v[170:171], v180 offset:30720
	ds_read_b64_tr_b16 v[172:173], v180 offset:31232
	v_pk_add_f32 v[254:255], v[254:255], v[42:43]
	v_cvt_pk_bf16_f32 v37, v40, v41
	v_pk_add_f32 v[254:255], v[254:255], v[44:45]
	v_cndmask_b32_e64 v106, 0, v37, s[72:73]
	v_cvt_pk_bf16_f32 v37, v42, v43
	v_cndmask_b32_e64 v107, 0, v37, s[72:73]
	s_waitcnt lgkmcnt(14)
	v_mfma_f32_32x32x16_bf16 v[84:99], v[158:161], v[118:121], v[84:99]
	ds_read_b64_tr_b16 v[174:175], v180 offset:27648
	ds_read_b64_tr_b16 v[176:177], v180 offset:28160
	v_pk_add_f32 v[254:255], v[254:255], v[46:47]
	v_cvt_pk_bf16_f32 v37, v44, v45
	v_pk_add_f32 v[254:255], v[254:255], v[48:49]
	v_cndmask_b32_e64 v100, 0, v37, s[72:73]
	v_cvt_pk_bf16_f32 v37, v46, v47
	v_cndmask_b32_e64 v101, 0, v37, s[72:73]
	s_waitcnt lgkmcnt(14)
	v_mfma_f32_32x32x16_bf16 v[68:83], v[154:157], v[114:117], v[68:83]
	ds_read_b64_tr_b16 v[178:179], v180 offset:31744
	ds_read_b64_tr_b16 v[180:181], v180 offset:32256
	v_pk_add_f32 v[254:255], v[254:255], v[50:51]
	v_add_f32_e32 v36, v254, v255
	v_mfma_f32_32x32x16_bf16 v[84:99], v[150:153], v[114:117], v[84:99]
	v_add_f32_e32 v150, 0, v36
	v_cvt_pk_bf16_f32 v36, v48, v49
	v_cndmask_b32_e64 v102, 0, v36, s[72:73]
	v_cvt_pk_bf16_f32 v36, v50, v51
	v_cndmask_b32_e64 v103, 0, v36, s[72:73]
	v_mov_b32_e32 v36, s85
	ds_read_b32 v37, v36 offset:16
	v_pk_add_f32 v[52:53], v[68:69], v[2:3] op_sel_hi:[1,0] neg_lo:[0,1] neg_hi:[0,1]
	v_pk_add_f32 v[54:55], v[70:71], v[2:3] op_sel_hi:[1,0] neg_lo:[0,1] neg_hi:[0,1]
	s_nop 2
	v_pk_add_f32 v[38:39], v[86:87], v[2:3] op_sel_hi:[1,0] neg_lo:[0,1] neg_hi:[0,1]
	v_pk_add_f32 v[56:57], v[72:73], v[2:3] op_sel_hi:[1,0] neg_lo:[0,1] neg_hi:[0,1]
	s_waitcnt lgkmcnt(0)
	v_readfirstlane_b32 s4, v37
	s_lshl_b32 s4, s4, 13
	s_and_b32 s4, s4, 0x7e000
	s_add_u32 s80, s77, s4
	s_addc_u32 s81, s78, 0
	s_add_i32 s4, s90, s95
	s_mov_b32 s76, m0
	s_mov_b32 m0, s4
	s_nop 0
	global_load_lds_dwordx4 v236, s[80:81]
	s_mov_b32 m0, s76
	ds_read_b32 v37, v36 offset:8
	v_pk_add_f32 v[40:41], v[88:89], v[2:3] op_sel_hi:[1,0] neg_lo:[0,1] neg_hi:[0,1]
	v_pk_add_f32 v[58:59], v[74:75], v[2:3] op_sel_hi:[1,0] neg_lo:[0,1] neg_hi:[0,1]
	v_pk_add_f32 v[42:43], v[90:91], v[2:3] op_sel_hi:[1,0] neg_lo:[0,1] neg_hi:[0,1]
	v_pk_add_f32 v[60:61], v[76:77], v[2:3] op_sel_hi:[1,0] neg_lo:[0,1] neg_hi:[0,1]
	s_waitcnt lgkmcnt(0)
	v_readfirstlane_b32 s4, v37
	s_lshl_b32 s4, s4, 13
	s_and_b32 s4, s4, 0x7e000
	s_add_u32 s80, s79, s4
	s_addc_u32 s81, s88, 0
	s_add_i32 s4, s84, s75
	s_mov_b32 s76, m0
	s_mov_b32 m0, s4
	s_nop 0
	global_load_lds_dwordx4 v237, s[80:81]
	s_mov_b32 m0, s76
	ds_read_b32 v36, v36 offset:4
	v_pk_add_f32 v[44:45], v[92:93], v[2:3] op_sel_hi:[1,0] neg_lo:[0,1] neg_hi:[0,1]
	v_pk_add_f32 v[62:63], v[78:79], v[2:3] op_sel_hi:[1,0] neg_lo:[0,1] neg_hi:[0,1]
	v_pk_add_f32 v[46:47], v[94:95], v[2:3] op_sel_hi:[1,0] neg_lo:[0,1] neg_hi:[0,1]
	v_pk_add_f32 v[64:65], v[80:81], v[2:3] op_sel_hi:[1,0] neg_lo:[0,1] neg_hi:[0,1]
	s_waitcnt lgkmcnt(0)
	v_readfirstlane_b32 s4, v36
	s_and_b32 s76, s4, 63
	s_sub_i32 s80, s94, s76
	v_pk_add_f32 v[36:37], v[84:85], v[2:3] op_sel_hi:[1,0] neg_lo:[0,1] neg_hi:[0,1]
	v_pk_add_f32 v[48:49], v[96:97], v[2:3] op_sel_hi:[1,0] neg_lo:[0,1] neg_hi:[0,1]
	v_pk_add_f32 v[66:67], v[82:83], v[2:3] op_sel_hi:[1,0] neg_lo:[0,1] neg_hi:[0,1]
	v_pk_add_f32 v[50:51], v[98:99], v[2:3] op_sel_hi:[1,0] neg_lo:[0,1] neg_hi:[0,1]
	s_cmp_gt_i32 s80, 2
	s_cbranch_scc1 .LBB0_1434
	v_lshl_add_u32 v99, s80, 8, v183
	ds_read_b32 v68, v99 offset:256
	ds_read_b32 v70, v99 offset:128
	ds_read_b32 v69, v99 offset:252
	ds_read_b32 v71, v99 offset:124
	ds_read_b32 v72, v99 offset:248
	ds_read_b32 v74, v99 offset:120
	ds_read_b32 v73, v99 offset:244
	ds_read_b32 v75, v99 offset:116
	ds_read_b32 v76, v99 offset:224
	ds_read_b32 v78, v99 offset:96
	ds_read_b32 v77, v99 offset:220
	ds_read_b32 v79, v99 offset:92
	ds_read_b32 v80, v99 offset:216
	ds_read_b32 v82, v99 offset:88
	ds_read_b32 v81, v99 offset:212
	ds_read_b32 v83, v99 offset:84
	ds_read_b32 v84, v99 offset:192
	ds_read_b32 v86, v99 offset:64
	ds_read_b32 v85, v99 offset:188
	ds_read_b32 v87, v99 offset:60
	ds_read_b32 v88, v99 offset:184
	ds_read_b32 v90, v99 offset:56
	ds_read_b32 v89, v99 offset:180
	ds_read_b32 v91, v99 offset:52
	ds_read_b32 v92, v99 offset:160
	ds_read_b32 v94, v99 offset:32
	ds_read_b32 v93, v99 offset:156
	ds_read_b32 v95, v99 offset:28
	ds_read_b32 v96, v99 offset:152
	ds_read_b32 v98, v99 offset:24
	ds_read_b32 v97, v99 offset:148
	ds_read_b32 v99, v99 offset:20
	s_waitcnt lgkmcnt(14)
	v_pk_add_f32 v[52:53], v[52:53], v[68:69]
	v_pk_add_f32 v[54:55], v[54:55], v[72:73]
	v_pk_add_f32 v[56:57], v[56:57], v[76:77]
	v_pk_add_f32 v[58:59], v[58:59], v[80:81]
	s_waitcnt lgkmcnt(13)
	v_pk_add_f32 v[60:61], v[60:61], v[84:85]
	s_waitcnt lgkmcnt(9)
	v_pk_add_f32 v[62:63], v[62:63], v[88:89]
	s_waitcnt lgkmcnt(5)
	v_pk_add_f32 v[64:65], v[64:65], v[92:93]
	s_waitcnt lgkmcnt(1)
	v_pk_add_f32 v[66:67], v[66:67], v[96:97]
	v_pk_add_f32 v[36:37], v[36:37], v[70:71]
	v_pk_add_f32 v[38:39], v[38:39], v[74:75]
	v_pk_add_f32 v[40:41], v[40:41], v[78:79]
	v_pk_add_f32 v[42:43], v[42:43], v[82:83]
	v_pk_add_f32 v[44:45], v[44:45], v[86:87]
	v_pk_add_f32 v[46:47], v[46:47], v[90:91]
	v_pk_add_f32 v[48:49], v[48:49], v[94:95]
	s_waitcnt lgkmcnt(0)
	v_pk_add_f32 v[50:51], v[50:51], v[98:99]

.LBB0_1451:
	v_add_u32_e32 v192, s90, v239
	ds_read_b64_tr_b16 v[182:183], v192 offset:24576
	ds_read_b64_tr_b16 v[184:185], v192 offset:25088
	v_pk_add_f32 v[254:255], v[52:53], v[54:55]
	v_pk_add_f32 v[254:255], v[254:255], v[56:57]
	s_waitcnt lgkmcnt(3)
	v_mfma_f32_32x32x16_bf16 v[68:83], v[162:165], v[126:129], 0
	v_cvt_pk_bf16_f32 v52, v52, v53
	v_cndmask_b32_e64 v130, 0, v52, s[92:93]
	v_cvt_pk_bf16_f32 v52, v54, v55
	v_cndmask_b32_e64 v131, 0, v52, s[92:93]
	ds_read_b64_tr_b16 v[162:163], v192 offset:28672
	ds_read_b64_tr_b16 v[164:165], v192 offset:29184
	v_pk_add_f32 v[254:255], v[254:255], v[58:59]
	s_waitcnt lgkmcnt(4)
	v_mfma_f32_32x32x16_bf16 v[84:99], v[154:157], v[126:129], 0
	v_cvt_pk_bf16_f32 v53, v56, v57
	v_pk_add_f32 v[254:255], v[254:255], v[60:61]
	v_cndmask_b32_e64 v132, 0, v53, s[92:93]
	v_cvt_pk_bf16_f32 v53, v58, v59
	v_cndmask_b32_e64 v133, 0, v53, s[92:93]
	ds_read_b64_tr_b16 v[166:167], v192 offset:25600
	ds_read_b64_tr_b16 v[168:169], v192 offset:26112
	s_waitcnt lgkmcnt(11)
	v_mfma_f32_32x32x16_bf16 v[68:83], v[158:161], v[122:125], v[68:83]
	v_pk_add_f32 v[254:255], v[254:255], v[62:63]
	v_cvt_pk_bf16_f32 v53, v60, v61
	v_pk_add_f32 v[254:255], v[254:255], v[64:65]
	v_cndmask_b32_e64 v108, 0, v53, s[92:93]
	v_cvt_pk_bf16_f32 v53, v62, v63
	v_cndmask_b32_e64 v109, 0, v53, s[92:93]
	ds_read_b64_tr_b16 v[170:171], v192 offset:29696
	ds_read_b64_tr_b16 v[172:173], v192 offset:30208
	s_waitcnt lgkmcnt(12)
	v_mfma_f32_32x32x16_bf16 v[84:99], v[150:153], v[122:125], v[84:99]
	v_pk_add_f32 v[254:255], v[254:255], v[66:67]
	v_cvt_pk_bf16_f32 v53, v64, v65
	v_pk_add_f32 v[254:255], v[254:255], v[36:37]
	v_cndmask_b32_e64 v110, 0, v53, s[92:93]
	v_cvt_pk_bf16_f32 v53, v66, v67
	v_cndmask_b32_e64 v111, 0, v53, s[92:93]
	ds_read_b64_tr_b16 v[174:175], v192 offset:26624
	ds_read_b64_tr_b16 v[176:177], v192 offset:27136
	s_waitcnt lgkmcnt(13)
	v_mfma_f32_32x32x16_bf16 v[68:83], v[146:149], v[118:121], v[68:83]
	v_pk_add_f32 v[254:255], v[254:255], v[38:39]
	v_cvt_pk_bf16_f32 v36, v36, v37
	v_pk_add_f32 v[254:255], v[254:255], v[40:41]
	v_cndmask_b32_e64 v104, 0, v36, s[92:93]
	v_cvt_pk_bf16_f32 v36, v38, v39
	v_cndmask_b32_e64 v105, 0, v36, s[92:93]
	ds_read_b64_tr_b16 v[178:179], v192 offset:30720
	ds_read_b64_tr_b16 v[180:181], v192 offset:31232
	s_waitcnt lgkmcnt(14)
	v_mfma_f32_32x32x16_bf16 v[84:99], v[142:145], v[118:121], v[84:99]
	v_pk_add_f32 v[254:255], v[254:255], v[42:43]
	v_cvt_pk_bf16_f32 v37, v40, v41
	v_pk_add_f32 v[254:255], v[254:255], v[44:45]
	v_cndmask_b32_e64 v106, 0, v37, s[92:93]
	v_cvt_pk_bf16_f32 v37, v42, v43
	v_cndmask_b32_e64 v107, 0, v37, s[92:93]
	ds_read_b64_tr_b16 v[186:187], v192 offset:27648
	ds_read_b64_tr_b16 v[188:189], v192 offset:28160
	s_waitcnt lgkmcnt(14)
	v_mfma_f32_32x32x16_bf16 v[68:83], v[138:141], v[114:117], v[68:83]
	v_pk_add_f32 v[254:255], v[254:255], v[46:47]
	v_cvt_pk_bf16_f32 v37, v44, v45
	v_pk_add_f32 v[254:255], v[254:255], v[48:49]
	v_cndmask_b32_e64 v100, 0, v37, s[92:93]
	v_cvt_pk_bf16_f32 v37, v46, v47
	v_cndmask_b32_e64 v101, 0, v37, s[92:93]
	ds_read_b64_tr_b16 v[190:191], v192 offset:31744
	ds_read_b64_tr_b16 v[192:193], v192 offset:32256
	v_mfma_f32_32x32x16_bf16 v[84:99], v[134:137], v[114:117], v[84:99]
	v_pk_add_f32 v[254:255], v[254:255], v[50:51]
	v_add_f32_e32 v36, v254, v255
	v_add_f32_e32 v134, 0, v36
	v_cvt_pk_bf16_f32 v36, v48, v49
	v_cndmask_b32_e64 v102, 0, v36, s[92:93]
	v_cvt_pk_bf16_f32 v36, v50, v51
	v_cndmask_b32_e64 v103, 0, v36, s[92:93]
	s_add_i32 s72, s76, 1
	s_cmp_ge_u32 s72, s83
	s_cselect_b64 s[80:81], -1, 0
	s_and_b64 vcc, exec, s[80:81]
	s_cbranch_vccnz .LBB0_1453
	v_mov_b32_e32 v36, s5
	ds_read_b32 v36, v36 offset:12
	s_waitcnt lgkmcnt(0)
	v_readfirstlane_b32 s72, v36
	s_lshl_b32 s72, s72, 13
	s_and_b32 s72, s72, 0x7e000
	s_add_u32 s72, s77, s72
	s_addc_u32 s73, s78, 0
	s_add_i32 s85, s84, s95
	s_mov_b32 s86, m0
	s_mov_b32 m0, s85
	s_nop 0
	global_load_lds_dwordx4 v236, s[72:73]
	s_mov_b32 m0, s86

.LBB0_1462:
	v_add_u32_e32 v176, s84, v239
	ds_read_b64_tr_b16 v[190:191], v176 offset:24576
	ds_read_b64_tr_b16 v[192:193], v176 offset:25088
	v_pk_add_f32 v[254:255], v[52:53], v[54:55]
	v_pk_add_f32 v[254:255], v[254:255], v[56:57]
	s_waitcnt lgkmcnt(9)
	v_mfma_f32_32x32x16_bf16 v[68:83], v[162:165], v[126:129], 0
	v_cvt_pk_bf16_f32 v52, v52, v53
	v_cndmask_b32_e64 v130, 0, v52, s[72:73]
	v_cvt_pk_bf16_f32 v52, v54, v55
	v_cndmask_b32_e64 v131, 0, v52, s[72:73]
	ds_read_b64_tr_b16 v[194:195], v176 offset:28672
	ds_read_b64_tr_b16 v[196:197], v176 offset:29184
	v_pk_add_f32 v[254:255], v[254:255], v[58:59]
	s_waitcnt lgkmcnt(10)
	v_mfma_f32_32x32x16_bf16 v[84:99], v[154:157], v[126:129], 0
	v_cvt_pk_bf16_f32 v53, v56, v57
	v_pk_add_f32 v[254:255], v[254:255], v[60:61]
	v_cndmask_b32_e64 v132, 0, v53, s[72:73]
	v_cvt_pk_bf16_f32 v53, v58, v59
	v_cndmask_b32_e64 v133, 0, v53, s[72:73]
	ds_read_b64_tr_b16 v[186:187], v176 offset:25600
	ds_read_b64_tr_b16 v[188:189], v176 offset:26112
	s_waitcnt lgkmcnt(11)
	v_mfma_f32_32x32x16_bf16 v[68:83], v[158:161], v[122:125], v[68:83]
	v_pk_add_f32 v[254:255], v[254:255], v[62:63]
	v_cvt_pk_bf16_f32 v53, v60, v61
	v_pk_add_f32 v[254:255], v[254:255], v[64:65]
	v_cndmask_b32_e64 v108, 0, v53, s[72:73]
	v_cvt_pk_bf16_f32 v53, v62, v63
	v_cndmask_b32_e64 v109, 0, v53, s[72:73]
	ds_read_b64_tr_b16 v[182:183], v176 offset:29696
	ds_read_b64_tr_b16 v[184:185], v176 offset:30208
	s_waitcnt lgkmcnt(12)
	v_mfma_f32_32x32x16_bf16 v[84:99], v[150:153], v[122:125], v[84:99]
	v_pk_add_f32 v[254:255], v[254:255], v[66:67]
	v_cvt_pk_bf16_f32 v53, v64, v65
	v_pk_add_f32 v[254:255], v[254:255], v[36:37]
	v_cndmask_b32_e64 v110, 0, v53, s[72:73]
	v_cvt_pk_bf16_f32 v53, v66, v67
	v_cndmask_b32_e64 v111, 0, v53, s[72:73]
	ds_read_b64_tr_b16 v[178:179], v176 offset:26624
	ds_read_b64_tr_b16 v[180:181], v176 offset:27136
	s_waitcnt lgkmcnt(13)
	v_mfma_f32_32x32x16_bf16 v[68:83], v[146:149], v[118:121], v[68:83]
	v_pk_add_f32 v[254:255], v[254:255], v[38:39]
	v_cvt_pk_bf16_f32 v36, v36, v37
	v_pk_add_f32 v[254:255], v[254:255], v[40:41]
	v_cndmask_b32_e64 v104, 0, v36, s[72:73]
	v_cvt_pk_bf16_f32 v36, v38, v39
	v_cndmask_b32_e64 v105, 0, v36, s[72:73]
	ds_read_b64_tr_b16 v[166:167], v176 offset:30720
	ds_read_b64_tr_b16 v[168:169], v176 offset:31232
	s_waitcnt lgkmcnt(14)
	v_mfma_f32_32x32x16_bf16 v[84:99], v[142:145], v[118:121], v[84:99]
	v_pk_add_f32 v[254:255], v[254:255], v[42:43]
	v_cvt_pk_bf16_f32 v37, v40, v41
	v_pk_add_f32 v[254:255], v[254:255], v[44:45]
	v_cndmask_b32_e64 v106, 0, v37, s[72:73]
	v_cvt_pk_bf16_f32 v37, v42, v43
	v_cndmask_b32_e64 v107, 0, v37, s[72:73]
	ds_read_b64_tr_b16 v[170:171], v176 offset:27648
	ds_read_b64_tr_b16 v[172:173], v176 offset:28160
	s_waitcnt lgkmcnt(14)
	v_mfma_f32_32x32x16_bf16 v[68:83], v[138:141], v[114:117], v[68:83]
	v_pk_add_f32 v[254:255], v[254:255], v[46:47]
	v_cvt_pk_bf16_f32 v37, v44, v45
	v_pk_add_f32 v[254:255], v[254:255], v[48:49]
	v_cndmask_b32_e64 v100, 0, v37, s[72:73]
	v_cvt_pk_bf16_f32 v37, v46, v47
	v_cndmask_b32_e64 v101, 0, v37, s[72:73]
	ds_read_b64_tr_b16 v[174:175], v176 offset:31744
	ds_read_b64_tr_b16 v[176:177], v176 offset:32256
	v_mfma_f32_32x32x16_bf16 v[84:99], v[134:137], v[114:117], v[84:99]
	v_pk_add_f32 v[254:255], v[254:255], v[50:51]
	v_add_f32_e32 v36, v254, v255
	v_add_f32_e32 v243, 0, v36
	v_cvt_pk_bf16_f32 v36, v48, v49
	v_cndmask_b32_e64 v102, 0, v36, s[72:73]
	v_cvt_pk_bf16_f32 v36, v50, v51
	v_cndmask_b32_e64 v103, 0, v36, s[72:73]
	s_add_i32 s85, s76, 2
	s_cmp_ge_u32 s85, s83
	s_cselect_b64 s[90:91], -1, 0
	s_and_b64 vcc, exec, s[90:91]
	s_cbranch_vccnz .LBB0_1464
	v_mov_b32_e32 v36, s5
	ds_read_b32 v36, v36 offset:16
	s_waitcnt lgkmcnt(0)
	v_readfirstlane_b32 s84, v36
	s_lshl_b32 s84, s84, 13
	s_and_b32 s84, s84, 0x7e000
	s_add_u32 s86, s77, s84
	s_addc_u32 s87, s78, 0
	s_add_i32 s84, s4, s95
	s_mov_b32 s92, m0
	s_mov_b32 m0, s84
	s_nop 0
	global_load_lds_dwordx4 v236, s[86:87]
	s_mov_b32 m0, s92

.LBB0_1504:
	v_add_u32_e32 v170, s4, v239
	ds_read_b64_tr_b16 v[166:167], v170 offset:24576
	ds_read_b64_tr_b16 v[168:169], v170 offset:25088
	v_pk_add_f32 v[254:255], v[52:53], v[54:55]
	v_cvt_pk_bf16_f32 v52, v52, v53
	v_pk_add_f32 v[254:255], v[254:255], v[56:57]
	v_cndmask_b32_e64 v130, 0, v52, s[92:93]
	v_cvt_pk_bf16_f32 v52, v54, v55
	v_cndmask_b32_e64 v131, 0, v52, s[92:93]
	s_waitcnt lgkmcnt(3)
	v_mfma_f32_32x32x16_bf16 v[68:83], v[162:165], v[126:129], 0
	ds_read_b64_tr_b16 v[162:163], v170 offset:28672
	ds_read_b64_tr_b16 v[164:165], v170 offset:29184
	v_pk_add_f32 v[254:255], v[254:255], v[58:59]
	v_cvt_pk_bf16_f32 v53, v56, v57
	v_pk_add_f32 v[254:255], v[254:255], v[60:61]
	v_cndmask_b32_e64 v132, 0, v53, s[92:93]
	v_cvt_pk_bf16_f32 v53, v58, v59
	v_cndmask_b32_e64 v133, 0, v53, s[92:93]
	s_waitcnt lgkmcnt(4)
	v_mfma_f32_32x32x16_bf16 v[84:99], v[154:157], v[126:129], 0
	ds_read_b64_tr_b16 v[154:155], v170 offset:25600
	ds_read_b64_tr_b16 v[156:157], v170 offset:26112
	v_pk_add_f32 v[254:255], v[254:255], v[62:63]
	v_cvt_pk_bf16_f32 v53, v60, v61
	v_pk_add_f32 v[254:255], v[254:255], v[64:65]
	v_cndmask_b32_e64 v108, 0, v53, s[92:93]
	v_cvt_pk_bf16_f32 v53, v62, v63
	v_cndmask_b32_e64 v109, 0, v53, s[92:93]
	v_mfma_f32_32x32x16_bf16 v[68:83], v[158:161], v[122:125], v[68:83]
	ds_read_b64_tr_b16 v[158:159], v170 offset:29696
	ds_read_b64_tr_b16 v[160:161], v170 offset:30208
	v_pk_add_f32 v[254:255], v[254:255], v[66:67]
	v_cvt_pk_bf16_f32 v53, v64, v65
	v_pk_add_f32 v[254:255], v[254:255], v[36:37]
	v_cndmask_b32_e64 v110, 0, v53, s[92:93]
	v_cvt_pk_bf16_f32 v53, v66, v67
	v_cndmask_b32_e64 v111, 0, v53, s[92:93]
	v_mfma_f32_32x32x16_bf16 v[84:99], v[150:153], v[122:125], v[84:99]
	ds_read_b64_tr_b16 v[150:151], v170 offset:26624
	ds_read_b64_tr_b16 v[152:153], v170 offset:27136
	v_pk_add_f32 v[254:255], v[254:255], v[38:39]
	v_cvt_pk_bf16_f32 v36, v36, v37
	v_pk_add_f32 v[254:255], v[254:255], v[40:41]
	v_cndmask_b32_e64 v104, 0, v36, s[92:93]
	v_cvt_pk_bf16_f32 v36, v38, v39
	v_cndmask_b32_e64 v105, 0, v36, s[92:93]
	v_mfma_f32_32x32x16_bf16 v[68:83], v[146:149], v[118:121], v[68:83]
	ds_read_b64_tr_b16 v[146:147], v170 offset:30720
	ds_read_b64_tr_b16 v[148:149], v170 offset:31232
	v_pk_add_f32 v[254:255], v[254:255], v[42:43]
	v_cvt_pk_bf16_f32 v37, v40, v41
	v_pk_add_f32 v[254:255], v[254:255], v[44:45]
	v_cndmask_b32_e64 v106, 0, v37, s[92:93]
	v_cvt_pk_bf16_f32 v37, v42, v43
	v_cndmask_b32_e64 v107, 0, v37, s[92:93]
	v_mfma_f32_32x32x16_bf16 v[84:99], v[142:145], v[118:121], v[84:99]
	ds_read_b64_tr_b16 v[142:143], v170 offset:27648
	ds_read_b64_tr_b16 v[144:145], v170 offset:28160
	v_pk_add_f32 v[254:255], v[254:255], v[46:47]
	v_cvt_pk_bf16_f32 v37, v44, v45
	v_pk_add_f32 v[254:255], v[254:255], v[48:49]
	v_cndmask_b32_e64 v100, 0, v37, s[92:93]
	v_cvt_pk_bf16_f32 v37, v46, v47
	v_cndmask_b32_e64 v101, 0, v37, s[92:93]
	v_mfma_f32_32x32x16_bf16 v[68:83], v[138:141], v[114:117], v[68:83]
	ds_read_b64_tr_b16 v[138:139], v170 offset:31744
	ds_read_b64_tr_b16 v[140:141], v170 offset:32256
	v_pk_add_f32 v[254:255], v[254:255], v[50:51]
	v_add_f32_e32 v36, v254, v255
	v_mfma_f32_32x32x16_bf16 v[84:99], v[134:137], v[114:117], v[84:99]
	v_add_f32_e32 v134, 0, v36
	v_cvt_pk_bf16_f32 v36, v48, v49
	v_cndmask_b32_e64 v102, 0, v36, s[92:93]
	v_cvt_pk_bf16_f32 v36, v50, v51
	v_cndmask_b32_e64 v103, 0, v36, s[92:93]
	s_lshl_b32 s4, s83, 2
	s_add_i32 s4, s4, 0
	s_add_i32 s4, s4, 0x1d9fc
	v_mov_b32_e32 v36, s4
	ds_read_b32 v36, v36
	v_pk_add_f32 v[52:53], v[68:69], v[2:3] op_sel_hi:[1,0] neg_lo:[0,1] neg_hi:[0,1]
	v_pk_add_f32 v[54:55], v[70:71], v[2:3] op_sel_hi:[1,0] neg_lo:[0,1] neg_hi:[0,1]
	v_pk_add_f32 v[38:39], v[86:87], v[2:3] op_sel_hi:[1,0] neg_lo:[0,1] neg_hi:[0,1]
	v_pk_add_f32 v[56:57], v[72:73], v[2:3] op_sel_hi:[1,0] neg_lo:[0,1] neg_hi:[0,1]
	s_waitcnt lgkmcnt(0)
	v_readfirstlane_b32 s4, v36
	s_and_b32 s5, s4, 63
	s_sub_i32 s6, s94, s5
	v_pk_add_f32 v[36:37], v[84:85], v[2:3] op_sel_hi:[1,0] neg_lo:[0,1] neg_hi:[0,1]
	v_pk_add_f32 v[40:41], v[88:89], v[2:3] op_sel_hi:[1,0] neg_lo:[0,1] neg_hi:[0,1]
	v_pk_add_f32 v[58:59], v[74:75], v[2:3] op_sel_hi:[1,0] neg_lo:[0,1] neg_hi:[0,1]
	v_pk_add_f32 v[42:43], v[90:91], v[2:3] op_sel_hi:[1,0] neg_lo:[0,1] neg_hi:[0,1]
	v_pk_add_f32 v[60:61], v[76:77], v[2:3] op_sel_hi:[1,0] neg_lo:[0,1] neg_hi:[0,1]
	v_pk_add_f32 v[44:45], v[92:93], v[2:3] op_sel_hi:[1,0] neg_lo:[0,1] neg_hi:[0,1]
	v_pk_add_f32 v[62:63], v[78:79], v[2:3] op_sel_hi:[1,0] neg_lo:[0,1] neg_hi:[0,1]
	v_pk_add_f32 v[46:47], v[94:95], v[2:3] op_sel_hi:[1,0] neg_lo:[0,1] neg_hi:[0,1]
	v_pk_add_f32 v[64:65], v[80:81], v[2:3] op_sel_hi:[1,0] neg_lo:[0,1] neg_hi:[0,1]
	v_pk_add_f32 v[48:49], v[96:97], v[2:3] op_sel_hi:[1,0] neg_lo:[0,1] neg_hi:[0,1]
	v_pk_add_f32 v[66:67], v[82:83], v[2:3] op_sel_hi:[1,0] neg_lo:[0,1] neg_hi:[0,1]
	v_pk_add_f32 v[50:51], v[98:99], v[2:3] op_sel_hi:[1,0] neg_lo:[0,1] neg_hi:[0,1]
	s_cmp_gt_i32 s6, 2
	s_cbranch_scc1 .LBB0_1506
	s_lshl_b32 s6, s6, 8
	v_sub_u32_e32 v2, v234, v233
	s_add_i32 s6, s6, s33
	v_lshl_add_u32 v2, v2, 2, s6
	ds_read_b32 v68, v2 offset:256
	ds_read_b32 v70, v2 offset:128
	ds_read_b32 v69, v2 offset:252
	ds_read_b32 v71, v2 offset:124
	ds_read_b32 v72, v2 offset:248
	ds_read_b32 v74, v2 offset:120
	ds_read_b32 v73, v2 offset:244
	ds_read_b32 v75, v2 offset:116
	ds_read_b32 v76, v2 offset:224
	ds_read_b32 v78, v2 offset:96
	ds_read_b32 v77, v2 offset:220
	ds_read_b32 v79, v2 offset:92
	ds_read_b32 v80, v2 offset:216
	ds_read_b32 v82, v2 offset:88
	ds_read_b32 v81, v2 offset:212
	ds_read_b32 v83, v2 offset:84
	ds_read_b32 v84, v2 offset:192
	ds_read_b32 v86, v2 offset:64
	ds_read_b32 v85, v2 offset:188
	ds_read_b32 v87, v2 offset:60
	ds_read_b32 v88, v2 offset:184
	ds_read_b32 v90, v2 offset:56
	ds_read_b32 v89, v2 offset:180
	ds_read_b32 v91, v2 offset:52
	ds_read_b32 v92, v2 offset:160
	ds_read_b32 v94, v2 offset:32
	ds_read_b32 v93, v2 offset:156
	ds_read_b32 v95, v2 offset:28
	ds_read_b32 v96, v2 offset:152
	ds_read_b32 v98, v2 offset:24
	ds_read_b32 v97, v2 offset:148
	ds_read_b32 v99, v2 offset:20
	s_waitcnt lgkmcnt(14)
	v_pk_add_f32 v[52:53], v[52:53], v[68:69]
	v_pk_add_f32 v[54:55], v[54:55], v[72:73]
	v_pk_add_f32 v[56:57], v[56:57], v[76:77]
	v_pk_add_f32 v[58:59], v[58:59], v[80:81]
	s_waitcnt lgkmcnt(13)
	v_pk_add_f32 v[60:61], v[60:61], v[84:85]
	s_waitcnt lgkmcnt(9)
	v_pk_add_f32 v[62:63], v[62:63], v[88:89]
	s_waitcnt lgkmcnt(5)
	v_pk_add_f32 v[64:65], v[64:65], v[92:93]
	s_waitcnt lgkmcnt(1)
	v_pk_add_f32 v[66:67], v[66:67], v[96:97]
	v_pk_add_f32 v[36:37], v[36:37], v[70:71]
	v_pk_add_f32 v[38:39], v[38:39], v[74:75]
	v_pk_add_f32 v[40:41], v[40:41], v[78:79]
	v_pk_add_f32 v[42:43], v[42:43], v[82:83]
	v_pk_add_f32 v[44:45], v[44:45], v[86:87]
	v_pk_add_f32 v[46:47], v[46:47], v[90:91]
	v_pk_add_f32 v[48:49], v[48:49], v[94:95]
	s_waitcnt lgkmcnt(0)
	v_pk_add_f32 v[50:51], v[50:51], v[98:99]

; #define SBAR() __builtin_amdgcn_sched_barrier(0)
;   #define PKW(P,B) cvtpk_s(P[B],P[B+1])
;   #define PKW(P,B) cvtpk_s(P[B],P[B+1])
; template<bool WIN,int THRL> __device__ __forceinline__ void nsa_branch_pipe(const bf16*__restrict__ Kb,const bf16*__restrict__ Vb,const __attribute__((address_space(3))) int*tl,int NT,int qc,const bf16x8*qr,unsigned selbits, ...
;     ...
;   { float sacc=pB0[0]+pB0[1]; _Pragma("unroll") for(int r=2;r<16;++r)sacc+=pB0[r]; _Pragma("unroll") for(int r=0;r<16;++r)sacc+=pB1[r]; l_reg+=(amB?sacc:0.f);
;     pw0=(u32x4){PKW(pB0,0)&amB,PKW(pB0,2)&amB,PKW(pB0,4)&amB,PKW(pB0,6)&amB};pw1=(u32x4){PKW(pB0,8)&amB,PKW(pB0,10)&amB,PKW(pB0,12)&amB,PKW(pB0,14)&amB};pw2=(u32x4){PKW(pB1,0)&amB,PKW(pB1,2)&amB,PKW(pB1,4)&amB,PKW(pB1,6)&amB};pw3=(u32x4){PKW(pB1,8)&amB,PKW(pB1,10)&amB,PKW(pB1,12)&amB,PKW(pB1,14)&amB};
;     SBAR(); pv(o,vb0+sl_cur,PAF(0),PAF(1),PAF(2),PAF(3)); }
;     ...
;   {auto rr=__builtin_amdgcn_permlane32_swap(__float_as_uint(l_reg),__float_as_uint(l_reg),false,false);l_out=__uint_as_float(rr[0])+__uint_as_float(rr[1]);}
;   asm volatile("s_waitcnt lgkmcnt(0)\n\ts_barrier":::"memory");
; __device__ __forceinline__ void nsa_unit(int b, int g, int qc, const bf16* Q, const bf16* KV, const bf16* KC2, size_t kvstride, size_t kc2stride, const float* gates, const float* lutg, bf16* O, char* shm) {
;     ...
;       const float gs = gl[64 + lane]; stash_acc(stash, ob, lt > 0.f ? gs * __builtin_amdgcn_rcpf(lt) : 0.f, wsf, lane, r32, hi, false); }
.LBB0_1511:
	v_pk_add_f32 v[254:255], v[52:53], v[54:55]
	v_pk_add_f32 v[254:255], v[254:255], v[56:57]
	v_pk_add_f32 v[254:255], v[254:255], v[58:59]
	v_pk_add_f32 v[254:255], v[254:255], v[60:61]
	v_pk_add_f32 v[254:255], v[254:255], v[62:63]
	v_pk_add_f32 v[254:255], v[254:255], v[64:65]
	v_pk_add_f32 v[254:255], v[254:255], v[66:67]
	v_pk_add_f32 v[254:255], v[254:255], v[36:37]
	v_pk_add_f32 v[254:255], v[254:255], v[38:39]
	v_pk_add_f32 v[254:255], v[254:255], v[40:41]
	v_pk_add_f32 v[254:255], v[254:255], v[42:43]
	v_pk_add_f32 v[254:255], v[254:255], v[44:45]
	v_pk_add_f32 v[254:255], v[254:255], v[46:47]
	v_pk_add_f32 v[254:255], v[254:255], v[48:49]
	v_pk_add_f32 v[254:255], v[254:255], v[50:51]
	v_add_f32_e32 v68, v254, v255
	s_cmp_lg_u32 0, -1
	s_cselect_b32 s6, 0, 0
	v_cndmask_b32_e64 v68, 0, v68, s[4:5]
	v_cvt_pk_bf16_f32 v36, v36, v37
	s_addk_i32 s6, 0x6000
	v_add_f32_e32 v2, v2, v68
	v_cvt_pk_bf16_f32 v52, v52, v53
	v_cvt_pk_bf16_f32 v53, v54, v55
	v_cvt_pk_bf16_f32 v54, v56, v57
	v_cvt_pk_bf16_f32 v55, v58, v59
	v_cvt_pk_bf16_f32 v56, v60, v61
	v_cvt_pk_bf16_f32 v57, v62, v63
	v_cvt_pk_bf16_f32 v58, v64, v65
	v_cvt_pk_bf16_f32 v59, v66, v67
	v_cndmask_b32_e64 v36, 0, v36, s[4:5]
	v_cvt_pk_bf16_f32 v37, v38, v39
	v_cvt_pk_bf16_f32 v38, v40, v41
	v_cvt_pk_bf16_f32 v39, v42, v43
	v_cvt_pk_bf16_f32 v40, v44, v45
	v_cvt_pk_bf16_f32 v41, v46, v47
	v_cvt_pk_bf16_f32 v42, v48, v49
	v_cvt_pk_bf16_f32 v43, v50, v51
	v_add3_u32 v69, v231, s6, v112
	v_cndmask_b32_e64 v52, 0, v52, s[4:5]
	v_cndmask_b32_e64 v53, 0, v53, s[4:5]
	v_cndmask_b32_e64 v54, 0, v54, s[4:5]
	v_cndmask_b32_e64 v55, 0, v55, s[4:5]
	v_cndmask_b32_e64 v56, 0, v56, s[4:5]
	v_cndmask_b32_e64 v57, 0, v57, s[4:5]
	v_cndmask_b32_e64 v58, 0, v58, s[4:5]
	v_cndmask_b32_e64 v59, 0, v59, s[4:5]
	v_cndmask_b32_e64 v37, 0, v37, s[4:5]
	v_cndmask_b32_e64 v38, 0, v38, s[4:5]
	v_cndmask_b32_e64 v39, 0, v39, s[4:5]
	v_cndmask_b32_e64 v40, 0, v40, s[4:5]
	v_cndmask_b32_e64 v41, 0, v41, s[4:5]
	v_cndmask_b32_e64 v42, 0, v42, s[4:5]
	v_cndmask_b32_e64 v43, 0, v43, s[4:5]
	v_add3_u32 v68, v69, v210, s84
	ds_read_b64_tr_b16 v[44:45],v68 offset:0
	ds_read_b64_tr_b16 v[46:47],v68 offset:512
	ds_read_b64_tr_b16 v[48:49],v68 offset:1024
	ds_read_b64_tr_b16 v[50:51],v68 offset:1536
	ds_read_b64_tr_b16 v[60:61],v68 offset:2048
	ds_read_b64_tr_b16 v[62:63],v68 offset:2560
	ds_read_b64_tr_b16 v[64:65],v68 offset:3072
	ds_read_b64_tr_b16 v[66:67],v68 offset:3584
	s_waitcnt lgkmcnt(0)
	s_nop 0
	v_mfma_f32_32x32x16_bf16 v[20:35], v[52:55], v[44:47], v[20:35]
	ds_read_b64_tr_b16 v[44:45],v68 offset:4096
	ds_read_b64_tr_b16 v[46:47],v68 offset:4608
	v_mfma_f32_32x32x16_bf16 v[20:35], v[56:59], v[48:51], v[20:35]
	ds_read_b64_tr_b16 v[48:49],v68 offset:5120
	ds_read_b64_tr_b16 v[50:51],v68 offset:5632
	v_mfma_f32_32x32x16_bf16 v[20:35], v[36:39], v[60:63], v[20:35]
	ds_read_b64_tr_b16 v[60:61],v68 offset:6144
	ds_read_b64_tr_b16 v[62:63],v68 offset:6656
	v_mfma_f32_32x32x16_bf16 v[20:35], v[40:43], v[64:67], v[20:35]
	ds_read_b64_tr_b16 v[64:65],v68 offset:7168
	ds_read_b64_tr_b16 v[66:67],v68 offset:7680
	s_waitcnt lgkmcnt(0)
	v_mfma_f32_32x32x16_bf16 v[4:19], v[52:55], v[44:47], v[4:19]
	s_waitcnt lgkmcnt(0)
	s_barrier
	v_mfma_f32_32x32x16_bf16 v[4:19], v[56:59], v[48:51], v[4:19]
	v_mfma_f32_32x32x16_bf16 v[4:19], v[36:39], v[60:63], v[4:19]
	v_mov_b32_e32 v36, v2
	s_nop 1
	v_permlane32_swap_b32_e32 v2, v36
	v_mfma_f32_32x32x16_bf16 v[4:19], v[40:43], v[64:67], v[4:19]
	s_and_saveexec_b64 s[4:5], s[2:3]
	s_cbranch_execz .LBB0_1513
	v_add_f32_e32 v2, v2, v36
	ds_read_b32 v36, v227 offset:256
	v_cmp_lt_f32_e32 vcc, 0, v2
	v_rcp_f32_e32 v2, v2
	v_readlane_b32 s6, v252, 33
	s_waitcnt lgkmcnt(0)
	v_mul_f32_e32 v2, v2, v36
	v_lshl_add_u32 v37, v212, 2, s6
	v_cndmask_b32_e32 v2, 0, v2, vcc
	ds_write_b32 v37, v2 offset:49152

.LBB0_1519:
	v_add_u32_e32 v2, s72, v241
	ds_read_b64_tr_b16 v[8:9], v2 offset:24576
	ds_read_b64_tr_b16 v[10:11], v2 offset:25088
	v_pk_add_f32 v[254:255], v[66:67], v[68:69]
	v_cvt_pk_bf16_f32 v5, v66, v67
	v_pk_add_f32 v[254:255], v[254:255], v[70:71]
	v_cndmask_b32_e64 v142, 0, v5, s[92:93]
	v_cvt_pk_bf16_f32 v5, v68, v69
	v_cndmask_b32_e64 v143, 0, v5, s[92:93]
	s_waitcnt lgkmcnt(9)
	v_mfma_f32_32x32x16_bf16 v[82:97], v[174:177], v[126:129], 0
	ds_read_b64_tr_b16 v[12:13], v2 offset:28672
	ds_read_b64_tr_b16 v[14:15], v2 offset:29184
	v_pk_add_f32 v[254:255], v[254:255], v[72:73]
	v_pk_add_f32 v[254:255], v[254:255], v[74:75]
	v_cvt_pk_bf16_f32 v4, v70, v71
	v_cndmask_b32_e64 v144, 0, v4, s[92:93]
	v_cvt_pk_bf16_f32 v4, v72, v73
	v_cndmask_b32_e64 v145, 0, v4, s[92:93]
	s_waitcnt lgkmcnt(10)
	v_mfma_f32_32x32x16_bf16 v[98:113], v[166:169], v[126:129], 0
	ds_read_b64_tr_b16 v[4:5], v2 offset:25600
	ds_read_b64_tr_b16 v[6:7], v2 offset:26112
	v_pk_add_f32 v[254:255], v[254:255], v[76:77]
	v_cvt_pk_bf16_f32 v17, v74, v75
	v_pk_add_f32 v[254:255], v[254:255], v[78:79]
	v_cndmask_b32_e64 v138, 0, v17, s[92:93]
	v_cvt_pk_bf16_f32 v17, v76, v77
	v_cndmask_b32_e64 v139, 0, v17, s[92:93]
	s_waitcnt lgkmcnt(11)
	v_mfma_f32_32x32x16_bf16 v[82:97], v[170:173], v[122:125], v[82:97]
	ds_read_b64_tr_b16 v[166:167], v2 offset:29696
	ds_read_b64_tr_b16 v[168:169], v2 offset:30208
	v_pk_add_f32 v[254:255], v[254:255], v[80:81]
	v_cvt_pk_bf16_f32 v17, v78, v79
	v_pk_add_f32 v[254:255], v[254:255], v[50:51]
	v_cndmask_b32_e64 v140, 0, v17, s[92:93]
	v_cvt_pk_bf16_f32 v17, v80, v81
	v_cndmask_b32_e64 v141, 0, v17, s[92:93]
	s_waitcnt lgkmcnt(12)
	v_mfma_f32_32x32x16_bf16 v[98:113], v[162:165], v[122:125], v[98:113]
	ds_read_b64_tr_b16 v[162:163], v2 offset:26624
	ds_read_b64_tr_b16 v[164:165], v2 offset:27136
	v_pk_add_f32 v[254:255], v[254:255], v[52:53]
	v_cvt_pk_bf16_f32 v17, v50, v51
	v_pk_add_f32 v[254:255], v[254:255], v[54:55]
	v_cndmask_b32_e64 v134, 0, v17, s[92:93]
	v_cvt_pk_bf16_f32 v17, v52, v53
	v_cndmask_b32_e64 v135, 0, v17, s[92:93]
	s_waitcnt lgkmcnt(13)
	v_mfma_f32_32x32x16_bf16 v[82:97], v[158:161], v[118:121], v[82:97]
	ds_read_b64_tr_b16 v[158:159], v2 offset:30720
	ds_read_b64_tr_b16 v[160:161], v2 offset:31232
	v_pk_add_f32 v[254:255], v[254:255], v[56:57]
	v_cvt_pk_bf16_f32 v17, v54, v55
	v_pk_add_f32 v[254:255], v[254:255], v[58:59]
	v_cndmask_b32_e64 v136, 0, v17, s[92:93]
	v_cvt_pk_bf16_f32 v17, v56, v57
	v_cndmask_b32_e64 v137, 0, v17, s[92:93]
	s_waitcnt lgkmcnt(14)
	v_mfma_f32_32x32x16_bf16 v[98:113], v[154:157], v[118:121], v[98:113]
	ds_read_b64_tr_b16 v[154:155], v2 offset:27648
	ds_read_b64_tr_b16 v[156:157], v2 offset:28160
	v_pk_add_f32 v[254:255], v[254:255], v[60:61]
	v_cvt_pk_bf16_f32 v17, v58, v59
	v_pk_add_f32 v[254:255], v[254:255], v[62:63]
	v_cndmask_b32_e64 v130, 0, v17, s[92:93]
	v_cvt_pk_bf16_f32 v17, v60, v61
	v_cndmask_b32_e64 v131, 0, v17, s[92:93]
	s_waitcnt lgkmcnt(14)
	v_mfma_f32_32x32x16_bf16 v[82:97], v[150:153], v[114:117], v[82:97]
	ds_read_b64_tr_b16 v[150:151], v2 offset:31744
	ds_read_b64_tr_b16 v[152:153], v2 offset:32256
	v_pk_add_f32 v[254:255], v[254:255], v[64:65]
	v_cvt_pk_bf16_f32 v16, v62, v63
	v_add_f32_e32 v2, v254, v255
	v_cndmask_b32_e64 v132, 0, v16, s[92:93]
	v_cvt_pk_bf16_f32 v16, v64, v65
	v_add_f32_e32 v2, 0, v2
	v_cndmask_b32_e64 v133, 0, v16, s[92:93]
	v_mfma_f32_32x32x16_bf16 v[98:113], v[146:149], v[114:117], v[98:113]
	v_mov_b32_e32 v16, s85
	ds_read_b32 v17, v16 offset:12
	v_add_f32_e64 v66, v82, -v210
	v_add_f32_e64 v67, v83, -v210
	s_nop 7
	v_pk_add_f32 v[50:51], v[98:99], v[210:211] op_sel_hi:[1,0] neg_lo:[0,1] neg_hi:[0,1]
	v_pk_add_f32 v[68:69], v[84:85], v[210:211] op_sel_hi:[1,0] neg_lo:[0,1] neg_hi:[0,1]
	v_pk_add_f32 v[52:53], v[100:101], v[210:211] op_sel_hi:[1,0] neg_lo:[0,1] neg_hi:[0,1]
	s_waitcnt lgkmcnt(0)
	v_readfirstlane_b32 s4, v17
	s_lshl_b32 s4, s4, 13
	s_and_b32 s4, s4, 0x7e000
	s_add_u32 s72, s89, s4
	s_addc_u32 s73, s0, 0
	s_add_i32 s4, s91, s75
	s_mov_b32 s76, m0
	s_mov_b32 m0, s4
	s_nop 0
	global_load_lds_dwordx4 v238, s[72:73]
	s_mov_b32 m0, s76
	ds_read_b32 v17, v16 offset:4
	v_pk_add_f32 v[70:71], v[86:87], v[210:211] op_sel_hi:[1,0] neg_lo:[0,1] neg_hi:[0,1]
	v_pk_add_f32 v[54:55], v[102:103], v[210:211] op_sel_hi:[1,0] neg_lo:[0,1] neg_hi:[0,1]
	v_pk_add_f32 v[72:73], v[88:89], v[210:211] op_sel_hi:[1,0] neg_lo:[0,1] neg_hi:[0,1]
	v_pk_add_f32 v[56:57], v[104:105], v[210:211] op_sel_hi:[1,0] neg_lo:[0,1] neg_hi:[0,1]
	s_waitcnt lgkmcnt(0)
	v_readfirstlane_b32 s4, v17
	s_lshl_b32 s4, s4, 13
	s_and_b32 s4, s4, 0x7e000
	s_add_u32 s72, s1, s4
	s_addc_u32 s73, s74, 0
	s_add_i32 s4, s90, s95
	s_mov_b32 s76, m0
	s_mov_b32 m0, s4
	s_nop 0
	global_load_lds_dwordx4 v239, s[72:73]
	s_mov_b32 m0, s76
	ds_read_b32 v16, v16
	v_pk_add_f32 v[74:75], v[90:91], v[210:211] op_sel_hi:[1,0] neg_lo:[0,1] neg_hi:[0,1]
	v_pk_add_f32 v[58:59], v[106:107], v[210:211] op_sel_hi:[1,0] neg_lo:[0,1] neg_hi:[0,1]
	v_pk_add_f32 v[76:77], v[92:93], v[210:211] op_sel_hi:[1,0] neg_lo:[0,1] neg_hi:[0,1]
	v_pk_add_f32 v[60:61], v[108:109], v[210:211] op_sel_hi:[1,0] neg_lo:[0,1] neg_hi:[0,1]
	s_waitcnt lgkmcnt(0)
	v_readfirstlane_b32 s4, v16
	s_and_b32 s72, s4, 63
	s_sub_i32 s73, s94, s72
	v_pk_add_f32 v[78:79], v[94:95], v[210:211] op_sel_hi:[1,0] neg_lo:[0,1] neg_hi:[0,1]
	v_pk_add_f32 v[62:63], v[110:111], v[210:211] op_sel_hi:[1,0] neg_lo:[0,1] neg_hi:[0,1]
	v_pk_add_f32 v[80:81], v[96:97], v[210:211] op_sel_hi:[1,0] neg_lo:[0,1] neg_hi:[0,1]
	v_pk_add_f32 v[64:65], v[112:113], v[210:211] op_sel_hi:[1,0] neg_lo:[0,1] neg_hi:[0,1]
	s_cmp_gt_i32 s73, 2
	s_cbranch_scc0 .LBB0_1535
	s_cmp_lg_u32 s94, s72
	s_cbranch_scc0 .LBB0_1536

.LBB0_1526:
	s_add_i32 s4, s90, 0x2000
	s_cmpk_lg_i32 s90, 0x4000
	s_cselect_b32 s84, s4, 0
	v_add_u32_e32 v16, s91, v241
	ds_read_b64_tr_b16 v[8:9], v16 offset:24576
	ds_read_b64_tr_b16 v[10:11], v16 offset:25088
	v_pk_add_f32 v[254:255], v[66:67], v[68:69]
	v_cvt_pk_bf16_f32 v5, v66, v67
	v_pk_add_f32 v[254:255], v[254:255], v[70:71]
	v_cndmask_b32_e64 v142, 0, v5, s[72:73]
	v_cvt_pk_bf16_f32 v5, v68, v69
	v_cndmask_b32_e64 v143, 0, v5, s[72:73]
	s_waitcnt lgkmcnt(9)
	v_mfma_f32_32x32x16_bf16 v[82:97], v[12:15], v[126:129], 0
	ds_read_b64_tr_b16 v[12:13], v16 offset:28672
	ds_read_b64_tr_b16 v[14:15], v16 offset:29184
	v_pk_add_f32 v[254:255], v[254:255], v[72:73]
	v_pk_add_f32 v[254:255], v[254:255], v[74:75]
	v_cvt_pk_bf16_f32 v4, v70, v71
	v_cndmask_b32_e64 v144, 0, v4, s[72:73]
	v_cvt_pk_bf16_f32 v4, v72, v73
	v_cndmask_b32_e64 v145, 0, v4, s[72:73]
	s_waitcnt lgkmcnt(10)
	v_mfma_f32_32x32x16_bf16 v[98:113], v[98:101], v[126:129], 0
	ds_read_b64_tr_b16 v[4:5], v16 offset:25600
	ds_read_b64_tr_b16 v[6:7], v16 offset:26112
	v_pk_add_f32 v[254:255], v[254:255], v[76:77]
	v_cvt_pk_bf16_f32 v66, v74, v75
	v_pk_add_f32 v[254:255], v[254:255], v[78:79]
	v_cndmask_b32_e64 v138, 0, v66, s[72:73]
	v_cvt_pk_bf16_f32 v66, v76, v77
	v_cndmask_b32_e64 v139, 0, v66, s[72:73]
	s_waitcnt lgkmcnt(11)
	v_mfma_f32_32x32x16_bf16 v[82:97], v[146:149], v[122:125], v[82:97]
	ds_read_b64_tr_b16 v[146:147], v16 offset:29696
	ds_read_b64_tr_b16 v[148:149], v16 offset:30208
	v_pk_add_f32 v[254:255], v[254:255], v[80:81]
	v_cvt_pk_bf16_f32 v66, v78, v79
	v_pk_add_f32 v[254:255], v[254:255], v[50:51]
	v_cndmask_b32_e64 v140, 0, v66, s[72:73]
	v_cvt_pk_bf16_f32 v66, v80, v81
	v_cndmask_b32_e64 v141, 0, v66, s[72:73]
	s_waitcnt lgkmcnt(12)
	v_mfma_f32_32x32x16_bf16 v[98:113], v[178:181], v[122:125], v[98:113]
	ds_read_b64_tr_b16 v[150:151], v16 offset:26624
	ds_read_b64_tr_b16 v[152:153], v16 offset:27136
	v_pk_add_f32 v[254:255], v[254:255], v[52:53]
	v_cvt_pk_bf16_f32 v50, v50, v51
	v_pk_add_f32 v[254:255], v[254:255], v[54:55]
	v_cndmask_b32_e64 v134, 0, v50, s[72:73]
	v_cvt_pk_bf16_f32 v50, v52, v53
	v_cndmask_b32_e64 v135, 0, v50, s[72:73]
	s_waitcnt lgkmcnt(13)
	v_mfma_f32_32x32x16_bf16 v[82:97], v[174:177], v[118:121], v[82:97]
	ds_read_b64_tr_b16 v[178:179], v16 offset:30720
	ds_read_b64_tr_b16 v[180:181], v16 offset:31232
	v_pk_add_f32 v[254:255], v[254:255], v[56:57]
	v_cvt_pk_bf16_f32 v50, v54, v55
	v_pk_add_f32 v[254:255], v[254:255], v[58:59]
	v_cndmask_b32_e64 v136, 0, v50, s[72:73]
	v_cvt_pk_bf16_f32 v50, v56, v57
	v_cndmask_b32_e64 v137, 0, v50, s[72:73]
	s_waitcnt lgkmcnt(14)
	v_mfma_f32_32x32x16_bf16 v[98:113], v[170:173], v[118:121], v[98:113]
	ds_read_b64_tr_b16 v[182:183], v16 offset:27648
	ds_read_b64_tr_b16 v[184:185], v16 offset:28160
	v_pk_add_f32 v[254:255], v[254:255], v[60:61]
	v_cvt_pk_bf16_f32 v50, v58, v59
	v_pk_add_f32 v[254:255], v[254:255], v[62:63]
	v_cndmask_b32_e64 v130, 0, v50, s[72:73]
	v_cvt_pk_bf16_f32 v50, v60, v61
	v_cndmask_b32_e64 v131, 0, v50, s[72:73]
	s_waitcnt lgkmcnt(14)
	v_mfma_f32_32x32x16_bf16 v[82:97], v[166:169], v[114:117], v[82:97]
	ds_read_b64_tr_b16 v[186:187], v16 offset:31744
	ds_read_b64_tr_b16 v[188:189], v16 offset:32256
	v_pk_add_f32 v[254:255], v[254:255], v[64:65]
	v_cvt_pk_bf16_f32 v17, v62, v63
	v_add_f32_e32 v16, v254, v255
	v_cndmask_b32_e64 v132, 0, v17, s[72:73]
	v_cvt_pk_bf16_f32 v17, v64, v65
	v_add_f32_e32 v16, 0, v16
	v_cndmask_b32_e64 v133, 0, v17, s[72:73]
	v_mfma_f32_32x32x16_bf16 v[98:113], v[162:165], v[114:117], v[98:113]
	v_mov_b32_e32 v17, s85
	ds_read_b32 v50, v17 offset:16
	v_add_f32_e64 v66, v82, -v210
	v_add_f32_e64 v67, v83, -v210
	v_add_f32_e64 v68, v84, -v210
	v_add_f32_e64 v69, v85, -v210
	s_nop 5
	v_pk_add_f32 v[52:53], v[100:101], v[210:211] op_sel_hi:[1,0] neg_lo:[0,1] neg_hi:[0,1]
	v_pk_add_f32 v[70:71], v[86:87], v[210:211] op_sel_hi:[1,0] neg_lo:[0,1] neg_hi:[0,1]
	s_waitcnt lgkmcnt(0)
	v_readfirstlane_b32 s4, v50
	s_lshl_b32 s4, s4, 13
	s_and_b32 s4, s4, 0x7e000
	s_add_u32 s80, s89, s4
	s_addc_u32 s81, s0, 0
	s_add_i32 s4, s90, s75
	s_mov_b32 s76, m0
	s_mov_b32 m0, s4
	s_nop 0
	global_load_lds_dwordx4 v238, s[80:81]
	s_mov_b32 m0, s76
	ds_read_b32 v50, v17 offset:8
	v_pk_add_f32 v[54:55], v[102:103], v[210:211] op_sel_hi:[1,0] neg_lo:[0,1] neg_hi:[0,1]
	v_pk_add_f32 v[72:73], v[88:89], v[210:211] op_sel_hi:[1,0] neg_lo:[0,1] neg_hi:[0,1]
	v_pk_add_f32 v[56:57], v[104:105], v[210:211] op_sel_hi:[1,0] neg_lo:[0,1] neg_hi:[0,1]
	v_pk_add_f32 v[74:75], v[90:91], v[210:211] op_sel_hi:[1,0] neg_lo:[0,1] neg_hi:[0,1]
	s_waitcnt lgkmcnt(0)
	v_readfirstlane_b32 s4, v50
	s_lshl_b32 s4, s4, 13
	s_and_b32 s4, s4, 0x7e000
	s_add_u32 s80, s1, s4
	s_addc_u32 s81, s74, 0
	s_add_i32 s4, s84, s95
	s_mov_b32 s76, m0
	s_mov_b32 m0, s4
	s_nop 0
	global_load_lds_dwordx4 v239, s[80:81]
	s_mov_b32 m0, s76
	ds_read_b32 v17, v17 offset:4
	v_pk_add_f32 v[50:51], v[98:99], v[210:211] op_sel_hi:[1,0] neg_lo:[0,1] neg_hi:[0,1]
	v_pk_add_f32 v[58:59], v[106:107], v[210:211] op_sel_hi:[1,0] neg_lo:[0,1] neg_hi:[0,1]
	v_pk_add_f32 v[76:77], v[92:93], v[210:211] op_sel_hi:[1,0] neg_lo:[0,1] neg_hi:[0,1]
	v_pk_add_f32 v[60:61], v[108:109], v[210:211] op_sel_hi:[1,0] neg_lo:[0,1] neg_hi:[0,1]
	s_waitcnt lgkmcnt(0)
	v_readfirstlane_b32 s4, v17
	s_and_b32 s76, s4, 63
	s_sub_i32 s80, s94, s76
	v_pk_add_f32 v[78:79], v[94:95], v[210:211] op_sel_hi:[1,0] neg_lo:[0,1] neg_hi:[0,1]
	v_pk_add_f32 v[62:63], v[110:111], v[210:211] op_sel_hi:[1,0] neg_lo:[0,1] neg_hi:[0,1]
	v_pk_add_f32 v[80:81], v[96:97], v[210:211] op_sel_hi:[1,0] neg_lo:[0,1] neg_hi:[0,1]
	v_pk_add_f32 v[64:65], v[112:113], v[210:211] op_sel_hi:[1,0] neg_lo:[0,1] neg_hi:[0,1]
	s_cmp_gt_i32 s80, 2
	s_cbranch_scc0 .LBB0_1537
	s_cmp_lg_u32 s94, s76
	s_cbranch_scc0 .LBB0_1538

.LBB0_1551:
	v_add_u32_e32 v17, s90, v241
	ds_read_b64_tr_b16 v[8:9], v17 offset:24576
	ds_read_b64_tr_b16 v[10:11], v17 offset:25088
	s_waitcnt lgkmcnt(3)
	v_mfma_f32_32x32x16_bf16 v[82:97], v[174:177], v[126:129], 0
	v_pk_add_f32 v[254:255], v[66:67], v[68:69]
	v_cvt_pk_bf16_f32 v5, v66, v67
	v_pk_add_f32 v[254:255], v[254:255], v[70:71]
	v_cndmask_b32_e64 v142, 0, v5, s[92:93]
	v_cvt_pk_bf16_f32 v5, v68, v69
	v_cndmask_b32_e64 v143, 0, v5, s[92:93]
	ds_read_b64_tr_b16 v[12:13], v17 offset:28672
	ds_read_b64_tr_b16 v[14:15], v17 offset:29184
	s_waitcnt lgkmcnt(4)
	v_mfma_f32_32x32x16_bf16 v[98:113], v[166:169], v[126:129], 0
	v_pk_add_f32 v[254:255], v[254:255], v[72:73]
	v_pk_add_f32 v[254:255], v[254:255], v[74:75]
	v_cvt_pk_bf16_f32 v4, v70, v71
	v_cndmask_b32_e64 v144, 0, v4, s[92:93]
	v_cvt_pk_bf16_f32 v4, v72, v73
	v_cndmask_b32_e64 v145, 0, v4, s[92:93]
	ds_read_b64_tr_b16 v[4:5], v17 offset:25600
	ds_read_b64_tr_b16 v[6:7], v17 offset:26112
	s_waitcnt lgkmcnt(11)
	v_mfma_f32_32x32x16_bf16 v[82:97], v[170:173], v[122:125], v[82:97]
	v_pk_add_f32 v[254:255], v[254:255], v[76:77]
	v_cvt_pk_bf16_f32 v67, v74, v75
	v_pk_add_f32 v[254:255], v[254:255], v[78:79]
	v_cndmask_b32_e64 v138, 0, v67, s[92:93]
	v_cvt_pk_bf16_f32 v67, v76, v77
	v_cndmask_b32_e64 v139, 0, v67, s[92:93]
	ds_read_b64_tr_b16 v[178:179], v17 offset:29696
	ds_read_b64_tr_b16 v[180:181], v17 offset:30208
	s_waitcnt lgkmcnt(12)
	v_mfma_f32_32x32x16_bf16 v[98:113], v[162:165], v[122:125], v[98:113]
	v_pk_add_f32 v[254:255], v[254:255], v[80:81]
	v_cvt_pk_bf16_f32 v67, v78, v79
	v_pk_add_f32 v[254:255], v[254:255], v[50:51]
	v_cndmask_b32_e64 v140, 0, v67, s[92:93]
	v_cvt_pk_bf16_f32 v67, v80, v81
	v_cndmask_b32_e64 v141, 0, v67, s[92:93]
	ds_read_b64_tr_b16 v[182:183], v17 offset:26624
	ds_read_b64_tr_b16 v[184:185], v17 offset:27136
	s_waitcnt lgkmcnt(13)
	v_mfma_f32_32x32x16_bf16 v[82:97], v[158:161], v[118:121], v[82:97]
	v_pk_add_f32 v[254:255], v[254:255], v[52:53]
	v_cvt_pk_bf16_f32 v50, v50, v51
	v_pk_add_f32 v[254:255], v[254:255], v[54:55]
	v_cndmask_b32_e64 v134, 0, v50, s[92:93]
	v_cvt_pk_bf16_f32 v50, v52, v53
	v_cndmask_b32_e64 v135, 0, v50, s[92:93]
	ds_read_b64_tr_b16 v[186:187], v17 offset:30720
	ds_read_b64_tr_b16 v[188:189], v17 offset:31232
	s_waitcnt lgkmcnt(14)
	v_mfma_f32_32x32x16_bf16 v[98:113], v[154:157], v[118:121], v[98:113]
	v_pk_add_f32 v[254:255], v[254:255], v[56:57]
	v_cvt_pk_bf16_f32 v51, v54, v55
	v_pk_add_f32 v[254:255], v[254:255], v[58:59]
	v_cndmask_b32_e64 v136, 0, v51, s[92:93]
	v_cvt_pk_bf16_f32 v51, v56, v57
	v_cndmask_b32_e64 v137, 0, v51, s[92:93]
	ds_read_b64_tr_b16 v[190:191], v17 offset:27648
	ds_read_b64_tr_b16 v[192:193], v17 offset:28160
	s_waitcnt lgkmcnt(14)
	v_mfma_f32_32x32x16_bf16 v[82:97], v[150:153], v[114:117], v[82:97]
	v_pk_add_f32 v[254:255], v[254:255], v[60:61]
	v_cvt_pk_bf16_f32 v51, v58, v59
	v_pk_add_f32 v[254:255], v[254:255], v[62:63]
	v_cndmask_b32_e64 v130, 0, v51, s[92:93]
	v_cvt_pk_bf16_f32 v51, v60, v61
	v_cndmask_b32_e64 v131, 0, v51, s[92:93]
	ds_read_b64_tr_b16 v[194:195], v17 offset:31744
	ds_read_b64_tr_b16 v[196:197], v17 offset:32256
	v_mfma_f32_32x32x16_bf16 v[98:113], v[146:149], v[114:117], v[98:113]
	v_pk_add_f32 v[254:255], v[254:255], v[64:65]
	v_cvt_pk_bf16_f32 v50, v62, v63
	v_add_f32_e32 v17, v254, v255
	v_cndmask_b32_e64 v132, 0, v50, s[92:93]
	v_cvt_pk_bf16_f32 v50, v64, v65
	v_add_f32_e32 v17, 0, v17
	v_cndmask_b32_e64 v133, 0, v50, s[92:93]
	s_add_i32 s72, s85, 1
	s_cmp_ge_u32 s72, s82
	s_cselect_b64 s[80:81], -1, 0
	s_and_b64 vcc, exec, s[80:81]
	s_cbranch_vccnz .LBB0_1553
	v_mov_b32_e32 v50, s5
	ds_read_b32 v50, v50 offset:12
	s_waitcnt lgkmcnt(0)
	v_readfirstlane_b32 s72, v50
	s_lshl_b32 s72, s72, 13
	s_and_b32 s72, s72, 0x7e000
	s_add_u32 s72, s89, s72
	s_addc_u32 s73, s0, 0
	s_add_i32 s76, s84, s75
	s_mov_b32 s86, m0
	s_mov_b32 m0, s76
	s_nop 0
	global_load_lds_dwordx4 v238, s[72:73]
	s_mov_b32 m0, s86

.LBB0_1562:
	v_add_u32_e32 v14, s84, v241
	ds_read_b64_tr_b16 v[190:191], v14 offset:24576
	ds_read_b64_tr_b16 v[192:193], v14 offset:25088
	s_waitcnt lgkmcnt(9)
	v_mfma_f32_32x32x16_bf16 v[82:97], v[174:177], v[126:129], 0
	v_pk_add_f32 v[254:255], v[66:67], v[68:69]
	v_cvt_pk_bf16_f32 v5, v66, v67
	v_pk_add_f32 v[254:255], v[254:255], v[70:71]
	v_cndmask_b32_e64 v142, 0, v5, s[72:73]
	v_cvt_pk_bf16_f32 v5, v68, v69
	v_cndmask_b32_e64 v143, 0, v5, s[72:73]
	ds_read_b64_tr_b16 v[194:195], v14 offset:28672
	ds_read_b64_tr_b16 v[196:197], v14 offset:29184
	s_waitcnt lgkmcnt(10)
	v_mfma_f32_32x32x16_bf16 v[98:113], v[166:169], v[126:129], 0
	v_pk_add_f32 v[254:255], v[254:255], v[72:73]
	v_cvt_pk_bf16_f32 v5, v70, v71
	v_pk_add_f32 v[254:255], v[254:255], v[74:75]
	v_cndmask_b32_e64 v144, 0, v5, s[72:73]
	v_cvt_pk_bf16_f32 v5, v72, v73
	v_cndmask_b32_e64 v145, 0, v5, s[72:73]
	ds_read_b64_tr_b16 v[186:187], v14 offset:25600
	ds_read_b64_tr_b16 v[188:189], v14 offset:26112
	s_waitcnt lgkmcnt(11)
	v_mfma_f32_32x32x16_bf16 v[82:97], v[170:173], v[122:125], v[82:97]
	v_pk_add_f32 v[254:255], v[254:255], v[76:77]
	v_cvt_pk_bf16_f32 v5, v74, v75
	v_pk_add_f32 v[254:255], v[254:255], v[78:79]
	v_cndmask_b32_e64 v138, 0, v5, s[72:73]
	v_cvt_pk_bf16_f32 v5, v76, v77
	v_cndmask_b32_e64 v139, 0, v5, s[72:73]
	ds_read_b64_tr_b16 v[182:183], v14 offset:29696
	ds_read_b64_tr_b16 v[184:185], v14 offset:30208
	s_waitcnt lgkmcnt(12)
	v_mfma_f32_32x32x16_bf16 v[98:113], v[162:165], v[122:125], v[98:113]
	v_pk_add_f32 v[254:255], v[254:255], v[80:81]
	v_cvt_pk_bf16_f32 v5, v78, v79
	v_pk_add_f32 v[254:255], v[254:255], v[50:51]
	v_cndmask_b32_e64 v140, 0, v5, s[72:73]
	v_cvt_pk_bf16_f32 v5, v80, v81
	v_cndmask_b32_e64 v141, 0, v5, s[72:73]
	ds_read_b64_tr_b16 v[178:179], v14 offset:26624
	ds_read_b64_tr_b16 v[180:181], v14 offset:27136
	s_waitcnt lgkmcnt(13)
	v_mfma_f32_32x32x16_bf16 v[82:97], v[158:161], v[118:121], v[82:97]
	v_pk_add_f32 v[254:255], v[254:255], v[52:53]
	v_pk_add_f32 v[254:255], v[254:255], v[54:55]
	v_cvt_pk_bf16_f32 v4, v50, v51
	v_cndmask_b32_e64 v134, 0, v4, s[72:73]
	v_cvt_pk_bf16_f32 v4, v52, v53
	v_cndmask_b32_e64 v135, 0, v4, s[72:73]
	ds_read_b64_tr_b16 v[4:5], v14 offset:30720
	ds_read_b64_tr_b16 v[6:7], v14 offset:31232
	s_waitcnt lgkmcnt(14)
	v_mfma_f32_32x32x16_bf16 v[98:113], v[154:157], v[118:121], v[98:113]
	v_pk_add_f32 v[254:255], v[254:255], v[56:57]
	v_pk_add_f32 v[254:255], v[254:255], v[58:59]
	v_cvt_pk_bf16_f32 v8, v54, v55
	v_cndmask_b32_e64 v136, 0, v8, s[72:73]
	v_cvt_pk_bf16_f32 v8, v56, v57
	v_cndmask_b32_e64 v137, 0, v8, s[72:73]
	ds_read_b64_tr_b16 v[8:9], v14 offset:27648
	ds_read_b64_tr_b16 v[10:11], v14 offset:28160
	s_waitcnt lgkmcnt(14)
	v_mfma_f32_32x32x16_bf16 v[82:97], v[150:153], v[114:117], v[82:97]
	v_pk_add_f32 v[254:255], v[254:255], v[60:61]
	v_pk_add_f32 v[254:255], v[254:255], v[62:63]
	v_cvt_pk_bf16_f32 v12, v58, v59
	v_cndmask_b32_e64 v130, 0, v12, s[72:73]
	v_cvt_pk_bf16_f32 v12, v60, v61
	v_cndmask_b32_e64 v131, 0, v12, s[72:73]
	ds_read_b64_tr_b16 v[12:13], v14 offset:31744
	ds_read_b64_tr_b16 v[14:15], v14 offset:32256
	v_mfma_f32_32x32x16_bf16 v[98:113], v[146:149], v[114:117], v[98:113]
	v_pk_add_f32 v[254:255], v[254:255], v[64:65]
	v_add_f32_e32 v50, v254, v255
	v_add_f32_e32 v242, 0, v50
	v_cvt_pk_bf16_f32 v50, v62, v63
	v_cndmask_b32_e64 v132, 0, v50, s[72:73]
	v_cvt_pk_bf16_f32 v50, v64, v65
	v_cndmask_b32_e64 v133, 0, v50, s[72:73]
	s_add_i32 s76, s85, 2
	s_cmp_ge_u32 s76, s82
	s_cselect_b64 s[90:91], -1, 0
	s_and_b64 vcc, exec, s[90:91]
	s_cbranch_vccnz .LBB0_1564
	v_mov_b32_e32 v50, s5
	ds_read_b32 v50, v50 offset:16
	s_waitcnt lgkmcnt(0)
	v_readfirstlane_b32 s84, v50
	s_lshl_b32 s84, s84, 13
	s_and_b32 s84, s84, 0x7e000
	s_add_u32 s86, s89, s84
	s_addc_u32 s87, s0, 0
	s_add_i32 s84, s4, s75
	s_mov_b32 s92, m0
	s_mov_b32 m0, s84
	s_nop 0
	global_load_lds_dwordx4 v238, s[86:87]
	s_mov_b32 m0, s92

.LBB0_1608:
	v_readlane_b32 s14, v252, 19
	v_readlane_b32 s12, v252, 36
	v_readlane_b32 s18, v252, 38
	v_readlane_b32 s15, v252, 20
	v_readlane_b32 s16, v252, 32
	v_readlane_b32 s63, v252, 35
	v_readlane_b32 s13, v252, 37
	v_readlane_b32 s19, v252, 39
	v_add_u32_e32 v2, s4, v241
	ds_read_b64_tr_b16 v[4:5], v2 offset:24576
	ds_read_b64_tr_b16 v[6:7], v2 offset:25088
	v_pk_add_f32 v[254:255], v[66:67], v[68:69]
	v_cvt_pk_bf16_f32 v9, v66, v67
	v_pk_add_f32 v[254:255], v[254:255], v[70:71]
	v_cndmask_b32_e64 v142, 0, v9, s[92:93]
	v_cvt_pk_bf16_f32 v9, v68, v69
	v_cndmask_b32_e64 v143, 0, v9, s[92:93]
	s_waitcnt lgkmcnt(3)
	v_mfma_f32_32x32x16_bf16 v[82:97], v[174:177], v[126:129], 0
	ds_read_b64_tr_b16 v[12:13], v2 offset:28672
	ds_read_b64_tr_b16 v[14:15], v2 offset:29184
	v_pk_add_f32 v[254:255], v[254:255], v[72:73]
	v_pk_add_f32 v[254:255], v[254:255], v[74:75]
	v_cvt_pk_bf16_f32 v8, v70, v71
	v_cndmask_b32_e64 v144, 0, v8, s[92:93]
	v_cvt_pk_bf16_f32 v8, v72, v73
	v_cndmask_b32_e64 v145, 0, v8, s[92:93]
	s_waitcnt lgkmcnt(4)
	v_mfma_f32_32x32x16_bf16 v[98:113], v[166:169], v[126:129], 0
	ds_read_b64_tr_b16 v[8:9], v2 offset:25600
	ds_read_b64_tr_b16 v[10:11], v2 offset:26112
	v_pk_add_f32 v[254:255], v[254:255], v[76:77]
	v_cvt_pk_bf16_f32 v17, v74, v75
	v_pk_add_f32 v[254:255], v[254:255], v[78:79]
	v_cndmask_b32_e64 v138, 0, v17, s[92:93]
	v_cvt_pk_bf16_f32 v17, v76, v77
	v_cndmask_b32_e64 v139, 0, v17, s[92:93]
	v_mfma_f32_32x32x16_bf16 v[82:97], v[170:173], v[122:125], v[82:97]
	ds_read_b64_tr_b16 v[126:127], v2 offset:29696
	ds_read_b64_tr_b16 v[128:129], v2 offset:30208
	v_pk_add_f32 v[254:255], v[254:255], v[80:81]
	v_cvt_pk_bf16_f32 v17, v78, v79
	v_pk_add_f32 v[254:255], v[254:255], v[50:51]
	v_cndmask_b32_e64 v140, 0, v17, s[92:93]
	v_cvt_pk_bf16_f32 v17, v80, v81
	v_cndmask_b32_e64 v141, 0, v17, s[92:93]
	v_mfma_f32_32x32x16_bf16 v[98:113], v[162:165], v[122:125], v[98:113]
	ds_read_b64_tr_b16 v[122:123], v2 offset:26624
	ds_read_b64_tr_b16 v[124:125], v2 offset:27136
	v_pk_add_f32 v[254:255], v[254:255], v[52:53]
	v_cvt_pk_bf16_f32 v17, v50, v51
	v_pk_add_f32 v[254:255], v[254:255], v[54:55]
	v_cndmask_b32_e64 v134, 0, v17, s[92:93]
	v_cvt_pk_bf16_f32 v17, v52, v53
	v_cndmask_b32_e64 v135, 0, v17, s[92:93]
	v_mfma_f32_32x32x16_bf16 v[82:97], v[158:161], v[118:121], v[82:97]
	ds_read_b64_tr_b16 v[158:159], v2 offset:30720
	ds_read_b64_tr_b16 v[160:161], v2 offset:31232
	v_pk_add_f32 v[254:255], v[254:255], v[56:57]
	v_cvt_pk_bf16_f32 v17, v54, v55
	v_pk_add_f32 v[254:255], v[254:255], v[58:59]
	v_cndmask_b32_e64 v136, 0, v17, s[92:93]
	v_cvt_pk_bf16_f32 v17, v56, v57
	v_cndmask_b32_e64 v137, 0, v17, s[92:93]
	v_mfma_f32_32x32x16_bf16 v[98:113], v[154:157], v[118:121], v[98:113]
	ds_read_b64_tr_b16 v[118:119], v2 offset:27648
	ds_read_b64_tr_b16 v[120:121], v2 offset:28160
	v_pk_add_f32 v[254:255], v[254:255], v[60:61]
	v_cvt_pk_bf16_f32 v17, v58, v59
	v_pk_add_f32 v[254:255], v[254:255], v[62:63]
	v_cndmask_b32_e64 v130, 0, v17, s[92:93]
	v_cvt_pk_bf16_f32 v17, v60, v61
	v_cndmask_b32_e64 v131, 0, v17, s[92:93]
	v_mfma_f32_32x32x16_bf16 v[82:97], v[150:153], v[114:117], v[82:97]
	ds_read_b64_tr_b16 v[150:151], v2 offset:31744
	ds_read_b64_tr_b16 v[152:153], v2 offset:32256
	v_pk_add_f32 v[254:255], v[254:255], v[64:65]
	v_cvt_pk_bf16_f32 v16, v62, v63
	v_add_f32_e32 v2, v254, v255
	v_cndmask_b32_e64 v132, 0, v16, s[92:93]
	v_cvt_pk_bf16_f32 v16, v64, v65
	v_add_f32_e32 v2, 0, v2
	v_cndmask_b32_e64 v133, 0, v16, s[92:93]
	v_mfma_f32_32x32x16_bf16 v[98:113], v[146:149], v[114:117], v[98:113]
	s_lshl_b32 s4, s82, 2
	s_add_i32 s4, s4, 0
	s_add_i32 s4, s4, 0x1dabc
	v_mov_b32_e32 v16, s4
	ds_read_b32 v16, v16
	v_pk_add_f32 v[66:67], v[82:83], v[210:211] op_sel_hi:[1,0] neg_lo:[0,1] neg_hi:[0,1]
	s_nop 5
	v_pk_add_f32 v[50:51], v[98:99], v[210:211] op_sel_hi:[1,0] neg_lo:[0,1] neg_hi:[0,1]
	v_pk_add_f32 v[68:69], v[84:85], v[210:211] op_sel_hi:[1,0] neg_lo:[0,1] neg_hi:[0,1]
	v_pk_add_f32 v[52:53], v[100:101], v[210:211] op_sel_hi:[1,0] neg_lo:[0,1] neg_hi:[0,1]
	s_waitcnt lgkmcnt(0)
	v_readfirstlane_b32 s4, v16
	s_and_b32 s6, s4, 63
	s_sub_i32 s5, s94, s6
	v_pk_add_f32 v[70:71], v[86:87], v[210:211] op_sel_hi:[1,0] neg_lo:[0,1] neg_hi:[0,1]
	v_pk_add_f32 v[54:55], v[102:103], v[210:211] op_sel_hi:[1,0] neg_lo:[0,1] neg_hi:[0,1]
	v_pk_add_f32 v[72:73], v[88:89], v[210:211] op_sel_hi:[1,0] neg_lo:[0,1] neg_hi:[0,1]
	v_pk_add_f32 v[56:57], v[104:105], v[210:211] op_sel_hi:[1,0] neg_lo:[0,1] neg_hi:[0,1]
	v_pk_add_f32 v[74:75], v[90:91], v[210:211] op_sel_hi:[1,0] neg_lo:[0,1] neg_hi:[0,1]
	v_pk_add_f32 v[58:59], v[106:107], v[210:211] op_sel_hi:[1,0] neg_lo:[0,1] neg_hi:[0,1]
	v_pk_add_f32 v[76:77], v[92:93], v[210:211] op_sel_hi:[1,0] neg_lo:[0,1] neg_hi:[0,1]
	v_pk_add_f32 v[60:61], v[108:109], v[210:211] op_sel_hi:[1,0] neg_lo:[0,1] neg_hi:[0,1]
	v_pk_add_f32 v[78:79], v[94:95], v[210:211] op_sel_hi:[1,0] neg_lo:[0,1] neg_hi:[0,1]
	v_pk_add_f32 v[62:63], v[110:111], v[210:211] op_sel_hi:[1,0] neg_lo:[0,1] neg_hi:[0,1]
	v_pk_add_f32 v[80:81], v[96:97], v[210:211] op_sel_hi:[1,0] neg_lo:[0,1] neg_hi:[0,1]
	v_pk_add_f32 v[64:65], v[112:113], v[210:211] op_sel_hi:[1,0] neg_lo:[0,1] neg_hi:[0,1]
	s_cmp_gt_i32 s5, 2
	s_cbranch_scc1 .LBB0_1610
	s_lshl_b32 s7, s5, 8
	v_sub_u32_e32 v16, v236, v235
	s_add_i32 s7, s7, s33
	v_lshl_add_u32 v111, v16, 2, s7
	ds_read_b32 v16, v111 offset:256
	ds_read_b32 v82, v111 offset:128
	ds_read_b32 v17, v111 offset:252
	ds_read_b32 v83, v111 offset:124
	ds_read_b32 v84, v111 offset:248
	ds_read_b32 v86, v111 offset:120
	ds_read_b32 v85, v111 offset:244
	ds_read_b32 v87, v111 offset:116
	ds_read_b32 v88, v111 offset:224
	ds_read_b32 v90, v111 offset:96
	ds_read_b32 v89, v111 offset:220
	ds_read_b32 v91, v111 offset:92
	ds_read_b32 v92, v111 offset:216
	ds_read_b32 v94, v111 offset:88
	ds_read_b32 v93, v111 offset:212
	ds_read_b32 v95, v111 offset:84
	ds_read_b32 v96, v111 offset:192
	ds_read_b32 v98, v111 offset:64
	ds_read_b32 v97, v111 offset:188
	ds_read_b32 v99, v111 offset:60
	ds_read_b32 v100, v111 offset:184
	ds_read_b32 v102, v111 offset:56
	ds_read_b32 v101, v111 offset:180
	ds_read_b32 v103, v111 offset:52
	ds_read_b32 v104, v111 offset:160
	ds_read_b32 v106, v111 offset:32
	ds_read_b32 v105, v111 offset:156
	ds_read_b32 v107, v111 offset:28
	ds_read_b32 v108, v111 offset:152
	ds_read_b32 v110, v111 offset:24
	ds_read_b32 v109, v111 offset:148
	ds_read_b32 v111, v111 offset:20
	s_waitcnt lgkmcnt(14)
	v_pk_add_f32 v[66:67], v[66:67], v[16:17]
	v_pk_add_f32 v[68:69], v[68:69], v[84:85]
	v_pk_add_f32 v[70:71], v[70:71], v[88:89]
	v_pk_add_f32 v[72:73], v[72:73], v[92:93]
	s_waitcnt lgkmcnt(13)
	v_pk_add_f32 v[74:75], v[74:75], v[96:97]
	s_waitcnt lgkmcnt(9)
	v_pk_add_f32 v[76:77], v[76:77], v[100:101]
	s_waitcnt lgkmcnt(5)
	v_pk_add_f32 v[78:79], v[78:79], v[104:105]
	s_waitcnt lgkmcnt(1)
	v_pk_add_f32 v[80:81], v[80:81], v[108:109]
	v_pk_add_f32 v[50:51], v[50:51], v[82:83]
	v_pk_add_f32 v[52:53], v[52:53], v[86:87]
	v_pk_add_f32 v[54:55], v[54:55], v[90:91]
	v_pk_add_f32 v[56:57], v[56:57], v[94:95]
	v_pk_add_f32 v[58:59], v[58:59], v[98:99]
	v_pk_add_f32 v[60:61], v[60:61], v[102:103]
	v_pk_add_f32 v[62:63], v[62:63], v[106:107]
	s_waitcnt lgkmcnt(0)
	v_pk_add_f32 v[64:65], v[64:65], v[110:111]

; #define SBAR() __builtin_amdgcn_sched_barrier(0)
;   #define PKW(P,B) cvtpk_s(P[B],P[B+1])
;   #define PKW(P,B) cvtpk_s(P[B],P[B+1])
; template<bool WIN,int THRL> __device__ __forceinline__ void nsa_branch_pipe(const bf16*__restrict__ Kb,const bf16*__restrict__ Vb,const __attribute__((address_space(3))) int*tl,int NT,int qc,const bf16x8*qr,unsigned selbits, ...
;     ...
;   { float sacc=pB0[0]+pB0[1]; _Pragma("unroll") for(int r=2;r<16;++r)sacc+=pB0[r]; _Pragma("unroll") for(int r=0;r<16;++r)sacc+=pB1[r]; l_reg+=(amB?sacc:0.f);
;     pw0=(u32x4){PKW(pB0,0)&amB,PKW(pB0,2)&amB,PKW(pB0,4)&amB,PKW(pB0,6)&amB};pw1=(u32x4){PKW(pB0,8)&amB,PKW(pB0,10)&amB,PKW(pB0,12)&amB,PKW(pB0,14)&amB};pw2=(u32x4){PKW(pB1,0)&amB,PKW(pB1,2)&amB,PKW(pB1,4)&amB,PKW(pB1,6)&amB};pw3=(u32x4){PKW(pB1,8)&amB,PKW(pB1,10)&amB,PKW(pB1,12)&amB,PKW(pB1,14)&amB};
;     SBAR(); pv(o,vb0+sl_cur,PAF(0),PAF(1),PAF(2),PAF(3)); }
;     ...
;   {auto rr=__builtin_amdgcn_permlane32_swap(__float_as_uint(l_reg),__float_as_uint(l_reg),false,false);l_out=__uint_as_float(rr[0])+__uint_as_float(rr[1]);}
;   asm volatile("s_waitcnt lgkmcnt(0)\n\ts_barrier":::"memory");
; __device__ __forceinline__ void nsa_unit(int b, int g, int qc, const bf16* Q, const bf16* KV, const bf16* KC2, size_t kvstride, size_t kc2stride, const float* gates, const float* lutg, bf16* O, char* shm) {
;     ...
;       const float gw = gl[128 + lane]; stash_acc(stash, ob, lt > 0.f ? gw * __builtin_amdgcn_rcpf(lt) : 0.f, wsf, lane, r32, hi, false); }
.LBB0_1618:
	v_pk_add_f32 v[254:255], v[66:67], v[68:69]
	v_pk_add_f32 v[254:255], v[254:255], v[70:71]
	v_pk_add_f32 v[254:255], v[254:255], v[72:73]
	v_pk_add_f32 v[254:255], v[254:255], v[74:75]
	v_pk_add_f32 v[254:255], v[254:255], v[76:77]
	v_pk_add_f32 v[254:255], v[254:255], v[78:79]
	v_pk_add_f32 v[254:255], v[254:255], v[80:81]
	v_pk_add_f32 v[254:255], v[254:255], v[50:51]
	v_pk_add_f32 v[254:255], v[254:255], v[52:53]
	v_pk_add_f32 v[254:255], v[254:255], v[54:55]
	v_pk_add_f32 v[254:255], v[254:255], v[56:57]
	v_pk_add_f32 v[254:255], v[254:255], v[58:59]
	v_pk_add_f32 v[254:255], v[254:255], v[60:61]
	v_pk_add_f32 v[254:255], v[254:255], v[62:63]
	v_pk_add_f32 v[254:255], v[254:255], v[64:65]
	v_add_f32_e32 v4, v254, v255
	v_cvt_pk_bf16_f32 v17, v58, v59
	s_cmp_lg_u32 0, -1
	v_cndmask_b32_e64 v4, 0, v4, s[4:5]
	v_cvt_pk_bf16_f32 v12, v50, v51
	v_cndmask_b32_e64 v50, 0, v17, s[4:5]
	v_cvt_pk_bf16_f32 v17, v60, v61
	s_cselect_b32 s6, 0, 0
	v_add_f32_e32 v2, v2, v4
	v_cvt_pk_bf16_f32 v4, v66, v67
	v_cndmask_b32_e64 v51, 0, v17, s[4:5]
	v_cvt_pk_bf16_f32 v17, v62, v63
	s_addk_i32 s6, 0x6000
	v_cndmask_b32_e64 v4, 0, v4, s[4:5]
	v_cvt_pk_bf16_f32 v5, v68, v69
	v_cvt_pk_bf16_f32 v6, v70, v71
	v_cvt_pk_bf16_f32 v7, v72, v73
	v_cvt_pk_bf16_f32 v8, v74, v75
	v_cvt_pk_bf16_f32 v9, v76, v77
	v_cvt_pk_bf16_f32 v10, v78, v79
	v_cvt_pk_bf16_f32 v11, v80, v81
	v_cvt_pk_bf16_f32 v13, v52, v53
	v_cvt_pk_bf16_f32 v14, v54, v55
	v_cvt_pk_bf16_f32 v15, v56, v57
	v_cndmask_b32_e64 v52, 0, v17, s[4:5]
	v_cvt_pk_bf16_f32 v17, v64, v65
	v_add3_u32 v16, v234, s6, v230
	v_cndmask_b32_e64 v5, 0, v5, s[4:5]
	v_cndmask_b32_e64 v6, 0, v6, s[4:5]
	v_cndmask_b32_e64 v7, 0, v7, s[4:5]
	v_cndmask_b32_e64 v8, 0, v8, s[4:5]
	v_cndmask_b32_e64 v9, 0, v9, s[4:5]
	v_cndmask_b32_e64 v10, 0, v10, s[4:5]
	v_cndmask_b32_e64 v11, 0, v11, s[4:5]
	v_cndmask_b32_e64 v12, 0, v12, s[4:5]
	v_cndmask_b32_e64 v13, 0, v13, s[4:5]
	v_cndmask_b32_e64 v14, 0, v14, s[4:5]
	v_cndmask_b32_e64 v15, 0, v15, s[4:5]
	v_cndmask_b32_e64 v53, 0, v17, s[4:5]
	v_add3_u32 v16, v16, v233, s84
	ds_read_b64_tr_b16 v[54:55],v16 offset:0
	ds_read_b64_tr_b16 v[56:57],v16 offset:512
	ds_read_b64_tr_b16 v[58:59],v16 offset:1024
	ds_read_b64_tr_b16 v[60:61],v16 offset:1536
	ds_read_b64_tr_b16 v[62:63],v16 offset:2048
	ds_read_b64_tr_b16 v[64:65],v16 offset:2560
	ds_read_b64_tr_b16 v[66:67],v16 offset:3072
	ds_read_b64_tr_b16 v[68:69],v16 offset:3584
	s_waitcnt lgkmcnt(0)
	s_nop 0
	v_mfma_f32_32x32x16_bf16 v[34:49], v[4:7], v[54:57], v[34:49]
	ds_read_b64_tr_b16 v[54:55],v16 offset:4096
	ds_read_b64_tr_b16 v[56:57],v16 offset:4608
	v_mfma_f32_32x32x16_bf16 v[34:49], v[8:11], v[58:61], v[34:49]
	ds_read_b64_tr_b16 v[58:59],v16 offset:5120
	ds_read_b64_tr_b16 v[60:61],v16 offset:5632
	v_mfma_f32_32x32x16_bf16 v[34:49], v[12:15], v[62:65], v[34:49]
	ds_read_b64_tr_b16 v[62:63],v16 offset:6144
	ds_read_b64_tr_b16 v[64:65],v16 offset:6656
	v_mfma_f32_32x32x16_bf16 v[34:49], v[50:53], v[66:69], v[34:49]
	ds_read_b64_tr_b16 v[66:67],v16 offset:7168
	ds_read_b64_tr_b16 v[68:69],v16 offset:7680
	s_waitcnt lgkmcnt(0)
	v_mfma_f32_32x32x16_bf16 v[18:33], v[4:7], v[54:57], v[18:33]
	s_waitcnt lgkmcnt(0)
	s_barrier
	v_mov_b32_e32 v4, v2
	s_nop 1
	v_permlane32_swap_b32_e32 v2, v4
	v_mfma_f32_32x32x16_bf16 v[18:33], v[8:11], v[58:61], v[18:33]
	v_mfma_f32_32x32x16_bf16 v[18:33], v[12:15], v[62:65], v[18:33]
	v_mfma_f32_32x32x16_bf16 v[18:33], v[50:53], v[66:69], v[18:33]
	s_and_saveexec_b64 s[4:5], s[2:3]
	s_cbranch_execz .LBB0_1368
	v_add_f32_e32 v2, v2, v4
	ds_read_b32 v4, v227 offset:512
	v_rcp_f32_e32 v5, v2
	v_cmp_lt_f32_e32 vcc, 0, v2
	v_lshl_add_u32 v6, v212, 2, s20
	s_waitcnt lgkmcnt(0)
	v_mul_f32_e32 v4, v5, v4
	v_cndmask_b32_e32 v2, 0, v4, vcc
	ds_write_b32 v6, v2 offset:49152
	s_branch .LBB0_1368

; __global__ void __launch_bounds__(NWAVES * 64, 2) fwd_kernel(Args args) {
	.amdhsa_kernel _Z10fwd_kernel4Args
		.amdhsa_group_segment_fixed_size 0
		.amdhsa_private_segment_fixed_size 0
		.amdhsa_kernarg_size 400
		.amdhsa_user_sgpr_count 2
		.amdhsa_user_sgpr_dispatch_ptr 0
		.amdhsa_user_sgpr_queue_ptr 0
		.amdhsa_user_sgpr_kernarg_segment_ptr 1
		.amdhsa_user_sgpr_dispatch_id 0
		.amdhsa_user_sgpr_kernarg_preload_length 0
		.amdhsa_user_sgpr_kernarg_preload_offset 0
		.amdhsa_user_sgpr_private_segment_size 0
		.amdhsa_uses_dynamic_stack 0
		.amdhsa_enable_private_segment 0
		.amdhsa_system_sgpr_workgroup_id_x 1
		.amdhsa_system_sgpr_workgroup_id_y 0
		.amdhsa_system_sgpr_workgroup_id_z 0
		.amdhsa_system_sgpr_workgroup_info 0
		.amdhsa_system_vgpr_workitem_id 0
		.amdhsa_next_free_vgpr 256
		.amdhsa_next_free_sgpr 100
		.amdhsa_accum_offset 256
		.amdhsa_reserve_vcc 1
		.amdhsa_float_round_mode_32 0
		.amdhsa_float_round_mode_16_64 0
		.amdhsa_float_denorm_mode_32 3
		.amdhsa_float_denorm_mode_16_64 3
		.amdhsa_dx10_clamp 1
		.amdhsa_ieee_mode 1
		.amdhsa_fp16_overflow 0
		.amdhsa_tg_split 0
		.amdhsa_exception_fp_ieee_invalid_op 0
		.amdhsa_exception_fp_denorm_src 0
		.amdhsa_exception_fp_ieee_div_zero 0
		.amdhsa_exception_fp_ieee_overflow 0
		.amdhsa_exception_fp_ieee_underflow 0
		.amdhsa_exception_fp_ieee_inexact 0
		.amdhsa_exception_int_div_zero 0
	.end_amdhsa_kernel

; __global__ void __launch_bounds__(NWAVES * 64, 2) fwd_kernel(Args args) {
amdhsa.kernels:
  - .agpr_count:     0
    .args:
      - .offset:         0
        .size:           144
        .value_kind:     by_value
      - .offset:         144
        .size:           4
        .value_kind:     hidden_block_count_x
      - .offset:         148
        .size:           4
        .value_kind:     hidden_block_count_y
      - .offset:         152
        .size:           4
        .value_kind:     hidden_block_count_z
      - .offset:         156
        .size:           2
        .value_kind:     hidden_group_size_x
      - .offset:         158
        .size:           2
        .value_kind:     hidden_group_size_y
      - .offset:         160
        .size:           2
        .value_kind:     hidden_group_size_z
      - .offset:         162
        .size:           2
        .value_kind:     hidden_remainder_x
      - .offset:         164
        .size:           2
        .value_kind:     hidden_remainder_y
      - .offset:         166
        .size:           2
        .value_kind:     hidden_remainder_z
      - .offset:         184
        .size:           8
        .value_kind:     hidden_global_offset_x
      - .offset:         192
        .size:           8
        .value_kind:     hidden_global_offset_y
      - .offset:         200
        .size:           8
        .value_kind:     hidden_global_offset_z
      - .offset:         208
        .size:           2
        .value_kind:     hidden_grid_dims
      - .offset:         264
        .size:           4
        .value_kind:     hidden_dynamic_lds_size
    .group_segment_fixed_size: 0
    .kernarg_segment_align: 8
    .kernarg_segment_size: 400
    .language:       OpenCL C
    .language_version:
      - 2
      - 0
    .max_flat_workgroup_size: 512
    .name:           _Z10fwd_kernel4Args
    .private_segment_fixed_size: 0
    .sgpr_count:     106
    .sgpr_spill_count: 119
    .symbol:         _Z10fwd_kernel4Args.kd
    .uniform_work_group_size: 1
    .uses_dynamic_stack: false
    .vgpr_count:     256
    .vgpr_spill_count: 0
    .wavefront_size: 64
